# GEMM K-loops: per-phase s_setprio 1/0 flips removed (all four GEMM phases)
# speedup vs baseline: 1.0125x; 1.0021x over previous
; #define PG8_STAGE(bufoff, gbase, voff) do { _Pragma("unroll") for (int _i = 0; _i < 2; ++_i) \
;         __builtin_amdgcn_global_load_lds((const unsigned*)((const char*)(gbase) + (voff)[_i]), (LAS unsigned*)(lds + (bufoff) + ldsw + _i * 8192), 16, 0, 0); } while (0)
; #define PG8_LDA(dst, b, h) do { _Pragma("unroll") for (int m = 0; m < 4; ++m) _Pragma("unroll") for (int k = 0; k < 2; ++k) dst[m][k] = *(const LAS bf16x8*)(lds + PG8_SA(b, h) + aoff + m * 2048 + k * 1024); } while (0)
; #define PG8_LDB(dst, b, h) do { _Pragma("unroll") for (int n = 0; n < 2; ++n) _Pragma("unroll") for (int k = 0; k < 2; ++k) dst[n][k] = *(const LAS bf16x8*)(lds + PG8_SB(b, h) + boff + n * 2048 + k * 1024); } while (0)
; #define PG8_MMA(ai, bj, At, Bt) do { __builtin_amdgcn_s_setprio(1); _Pragma("unroll") for (int m = 0; m < 4; ++m) _Pragma("unroll") for (int n = 0; n < 2; ++n) _Pragma("unroll") for (int k = 0; k < 2; ++k) \
;         acc[ai][bj][m][n] = __builtin_amdgcn_mfma_f32_16x16x32_bf16(Bt[n][k], At[m][k], acc[ai][bj][m][n], 0, 0, 0); __builtin_amdgcn_s_setprio(0); } while (0)
; #define PG8_WAIT_L(n) asm volatile("s_waitcnt lgkmcnt(" #n ")" ::: "memory")
; #define PG8_BAR __builtin_amdgcn_s_barrier()
; #define PG8_SCHED __builtin_amdgcn_sched_barrier(0)
; #define PG8_AOFF(u) do { const int _t = lt_tid(wvid); _Pragma("unroll") for (int _i = 0; _i < 2; ++_i) { int _R, _C; stage_rc(_t * 16 + _i * 8192, _R, _C); \
;         _Pragma("unroll") for (int _h = 0; _h < 2; ++_h) voffA[_h][_i] = (S.a_row(u, _h * HALF + _R) * (unsigned)K + (unsigned)(_C + (u).koff)) * 2u; } } while (0)
; template <class Epi, class Sched>
; __device__ __forceinline__ void gemm_phase(LAS unsigned char* lds, const bf16_t* Abase, const int K, const Sched& S, const Epi& E, const int wvid) {
;     ...
;             PG8_LDB(B0, 0, 0); PG8_SCHED; PG8_LDA(At, 0, 0); PG8_STAGE(PG8_SA(1, 1), a1, voffA[1]);
;             PG8_WAIT_L(8); PG8_BAR; PG8_WAIT_L(0); PG8_MMA(0, 0, At, B0); PG8_BAR; PG8_SCHED;
;             if (last && has_next) PG8_AOFF(nxt);
.LBB0_125:
	ds_read_b128 v[130:133], v193
	ds_read_b128 v[134:137], v193 offset:1024
	ds_read_b128 v[138:141], v193 offset:2048
	ds_read_b128 v[142:145], v193 offset:3072
	s_cmp_eq_u32 s61, 12
	s_cselect_b64 s[30:31], -1, 0
	s_add_i32 m0, s17, 0xc000
	s_add_u32 s28, s22, s4
	s_addc_u32 s29, s23, s5
	ds_read_b128 v[170:173], v194
	ds_read_b128 v[174:177], v194 offset:1024
	ds_read_b128 v[162:165], v194 offset:2048
	ds_read_b128 v[166:169], v194 offset:3072
	ds_read_b128 v[154:157], v194 offset:4096
	ds_read_b128 v[158:161], v194 offset:5120
	ds_read_b128 v[146:149], v194 offset:6144
	ds_read_b128 v[150:153], v194 offset:7168
	global_load_lds_dwordx4 v182, s[28:29]
	s_add_i32 m0, s17, 0xe000
	s_nop 0
	global_load_lds_dwordx4 v186, s[28:29]
	s_waitcnt lgkmcnt(8)
	s_barrier
	s_waitcnt lgkmcnt(0)
	s_waitcnt lgkmcnt(0)
	v_mfma_f32_16x16x32_bf16 v[126:129], v[130:133], v[170:173], v[126:129]
	v_mfma_f32_16x16x32_bf16 v[122:125], v[138:141], v[170:173], v[122:125]
	v_mfma_f32_16x16x32_bf16 v[118:121], v[130:133], v[162:165], v[118:121]
	v_mfma_f32_16x16x32_bf16 v[114:117], v[138:141], v[162:165], v[114:117]
	v_mfma_f32_16x16x32_bf16 v[102:105], v[130:133], v[154:157], v[102:105]
	v_mfma_f32_16x16x32_bf16 v[98:101], v[138:141], v[154:157], v[98:101]
	v_mfma_f32_16x16x32_bf16 v[86:89], v[130:133], v[146:149], v[86:89]
	v_mfma_f32_16x16x32_bf16 v[82:85], v[138:141], v[146:149], v[82:85]
	v_mfma_f32_16x16x32_bf16 v[126:129], v[134:137], v[174:177], v[126:129]
	v_mfma_f32_16x16x32_bf16 v[122:125], v[142:145], v[174:177], v[122:125]
	v_mfma_f32_16x16x32_bf16 v[118:121], v[134:137], v[166:169], v[118:121]
	v_mfma_f32_16x16x32_bf16 v[114:117], v[142:145], v[166:169], v[114:117]
	v_mfma_f32_16x16x32_bf16 v[102:105], v[134:137], v[158:161], v[102:105]
	v_mfma_f32_16x16x32_bf16 v[98:101], v[142:145], v[158:161], v[98:101]
	v_mfma_f32_16x16x32_bf16 v[86:89], v[134:137], v[150:153], v[86:89]
	v_mfma_f32_16x16x32_bf16 v[82:85], v[142:145], v[150:153], v[82:85]
	s_barrier
	s_and_b64 s[28:29], s[0:1], s[30:31]
	s_andn2_b64 vcc, exec, s[28:29]
	s_cbranch_vccnz .LBB0_127
	v_mbcnt_lo_u32_b32 v0, -1, 0
	v_mbcnt_hi_u32_b32 v0, -1, v0
	s_nop 0
	v_or_b32_e32 v0, s75, v0
	v_ashrrev_i32_e32 v183, 31, v0
	v_lshrrev_b32_e32 v183, 26, v183
	v_lshlrev_b32_e32 v182, 4, v0
	v_add_u32_e32 v183, v0, v183
	v_bfe_i32 v0, v0, 27, 1
	v_lshrrev_b32_e32 v0, 22, v0
	v_add_u32_e32 v0, v182, v0
	v_and_b32_e32 v0, 0xfffffc00, v0
	v_sub_u32_e32 v0, v182, v0
	v_lshrrev_b32_e32 v184, 4, v0
	v_bitop3_b32 v0, v184, v0, 32 bitop3:0x6c
	v_ashrrev_i32_e32 v185, 31, v0
	v_lshrrev_b32_e32 v185, 26, v185
	v_ashrrev_i32_e32 v183, 6, v183
	v_add_u32_e32 v185, v0, v185
	v_lshlrev_b32_e32 v184, 3, v183
	v_lshrrev_b32_e32 v186, 6, v185
	v_and_b32_e32 v185, 0xc0, v185
	v_and_b32_e32 v184, 0x1ffff0, v184
	v_lshlrev_b32_e32 v183, 5, v183
	v_sub_u32_e32 v0, v0, v185
	v_and_b32_e32 v183, 32, v183
	v_ashrrev_i16_sdwa v0, v216, sext(v0) dst_sel:DWORD dst_unused:UNUSED_PAD src0_sel:DWORD src1_sel:BYTE_0
	v_add_u32_e32 v184, s56, v184
	v_add_u32_e32 v182, 0x2000, v182
	v_add_u32_sdwa v0, v183, sext(v0) dst_sel:DWORD dst_unused:UNUSED_PAD src0_sel:DWORD src1_sel:WORD_0
	v_add_lshl_u32 v183, v184, v186, 11
	v_ashrrev_i32_e32 v184, 31, v182
	v_lshrrev_b32_e32 v184, 22, v184
	v_add_u32_e32 v184, v182, v184
	v_ashrrev_i32_e32 v184, 10, v184
	v_mul_i32_i24_e32 v185, 0x400, v184
	v_sub_u32_e32 v182, v182, v185
	v_lshrrev_b32_e32 v185, 4, v182
	v_bitop3_b32 v182, v185, v182, 32 bitop3:0x6c
	v_ashrrev_i32_e32 v186, 31, v182
	v_lshrrev_b32_e32 v186, 26, v186
	v_add_u32_e32 v186, v182, v186
	v_lshlrev_b32_e32 v185, 3, v184
	v_lshrrev_b32_e32 v187, 6, v186
	v_and_b32_e32 v186, 0xc0, v186
	v_and_b32_e32 v185, 0x1ffff0, v185
	v_lshlrev_b32_e32 v184, 5, v184
	v_sub_u32_e32 v182, v182, v186
	v_and_b32_e32 v184, 32, v184
	v_ashrrev_i16_sdwa v182, v216, sext(v182) dst_sel:DWORD dst_unused:UNUSED_PAD src0_sel:DWORD src1_sel:BYTE_0
	v_add_u32_e32 v185, s56, v185
	v_lshl_add_u32 v183, v0, 1, v183
	v_add_u32_sdwa v182, v184, sext(v182) dst_sel:DWORD dst_unused:UNUSED_PAD src0_sel:DWORD src1_sel:WORD_0
	v_add_lshl_u32 v184, v185, v187, 11
	v_add_u32_e32 v0, 0x40000, v183
	v_lshl_add_u32 v184, v182, 1, v184
	v_add_u32_e32 v186, 0x40000, v184
	v_mov_b32_e32 v187, v1
	v_mov_b64_e32 v[188:189], v[0:1]
	v_mov_b32_e32 v182, v0
	v_mov_b32_e32 v0, v183
	s_branch .LBB0_128

; #define PG8_STAGE(bufoff, gbase, voff) do { _Pragma("unroll") for (int _i = 0; _i < 2; ++_i) \
;         __builtin_amdgcn_global_load_lds((const unsigned*)((const char*)(gbase) + (voff)[_i]), (LAS unsigned*)(lds + (bufoff) + ldsw + _i * 8192), 16, 0, 0); } while (0)
; #define PG8_LDA(dst, b, h) do { _Pragma("unroll") for (int m = 0; m < 4; ++m) _Pragma("unroll") for (int k = 0; k < 2; ++k) dst[m][k] = *(const LAS bf16x8*)(lds + PG8_SA(b, h) + aoff + m * 2048 + k * 1024); } while (0)
; #define PG8_LDB(dst, b, h) do { _Pragma("unroll") for (int n = 0; n < 2; ++n) _Pragma("unroll") for (int k = 0; k < 2; ++k) dst[n][k] = *(const LAS bf16x8*)(lds + PG8_SB(b, h) + boff + n * 2048 + k * 1024); } while (0)
; #define PG8_MMA(ai, bj, At, Bt) do { __builtin_amdgcn_s_setprio(1); _Pragma("unroll") for (int m = 0; m < 4; ++m) _Pragma("unroll") for (int n = 0; n < 2; ++n) _Pragma("unroll") for (int k = 0; k < 2; ++k) \
;         acc[ai][bj][m][n] = __builtin_amdgcn_mfma_f32_16x16x32_bf16(Bt[n][k], At[m][k], acc[ai][bj][m][n], 0, 0, 0); __builtin_amdgcn_s_setprio(0); } while (0)
; #define PG8_WAIT_V(n) asm volatile("s_waitcnt vmcnt(" #n ")" ::: "memory")
; #define PG8_WAIT_L(n) asm volatile("s_waitcnt lgkmcnt(" #n ")" ::: "memory")
; #define PG8_BAR __builtin_amdgcn_s_barrier()
; #define PG8_SCHED __builtin_amdgcn_sched_barrier(0)
; template <class Epi, class Sched>
; __device__ __forceinline__ void gemm_phase(LAS unsigned char* lds, const bf16_t* Abase, const int K, const Sched& S, const Epi& E, const int wvid) {
;     ...
;             const char* a2 = last ? Ab : Ab + (size_t)(t + 2) * kstep; const char* b2 = last ? nB : cB + (size_t)(t + 2) * kstep;
;             const char* a3 = a2 + kstep; const char* b3 = b2 + kstep;
;             PG8_LDB(B1, 0, 1); PG8_STAGE(PG8_SB(0, 0), b2, voffB);
;             PG8_BAR; PG8_WAIT_L(0); PG8_MMA(0, 1, At, B1); PG8_BAR;
;             PG8_LDA(At, 0, 1); PG8_STAGE(PG8_SA(0, 0), a2, voffA[0]);
;             PG8_BAR; PG8_WAIT_L(0); PG8_MMA(1, 0, At, B0); PG8_BAR; PG8_SCHED;
;             PG8_STAGE(PG8_SB(0, 1), b2 + hstep, voffB);
;             PG8_WAIT_V(6); PG8_BAR; PG8_MMA(1, 1, At, B1); PG8_BAR;
;             PG8_LDB(B0, 1, 0); PG8_SCHED; PG8_LDA(At, 1, 0); PG8_STAGE(PG8_SA(0, 1), a2, voffA[1]);
.LBB0_128:
	s_add_u32 s28, s4, 0x100
	s_addc_u32 s29, s5, 0
	s_and_b64 s[34:35], s[30:31], exec
	s_cselect_b32 s34, 0, s28
	s_cselect_b32 s35, 0, s29
	s_add_u32 s34, s10, s34
	s_addc_u32 s35, s11, s35
	s_add_u32 s62, s59, s4
	s_addc_u32 s63, s60, s5
	s_add_i32 s64, 0, 0x14000
	s_and_b64 s[4:5], s[30:31], exec
	s_cselect_b32 s5, s25, s63
	s_cselect_b32 s4, s58, s62
	s_mov_b32 m0, s42
	v_add_u32_e32 v183, s64, v192
	v_lshl_add_u64 v[200:201], s[4:5], 0, v[178:179]
	ds_read_b128 v[196:199], v183
	ds_read_b128 v[224:227], v183 offset:1024
	ds_read_b128 v[228:231], v183 offset:2048
	ds_read_b128 v[232:235], v183 offset:3072
	global_load_lds_dwordx4 v[200:201], off
	v_lshl_add_u64 v[202:203], s[4:5], 0, v[180:181]
	s_mov_b32 m0, s43
	s_nop 0
	global_load_lds_dwordx4 v[202:203], off
	s_barrier
	s_waitcnt lgkmcnt(0)
	s_waitcnt lgkmcnt(0)
	v_mfma_f32_16x16x32_bf16 v[110:113], v[196:199], v[170:173], v[110:113]
	v_mfma_f32_16x16x32_bf16 v[106:109], v[228:231], v[170:173], v[106:109]
	v_mfma_f32_16x16x32_bf16 v[94:97], v[196:199], v[162:165], v[94:97]
	v_mfma_f32_16x16x32_bf16 v[90:93], v[228:231], v[162:165], v[90:93]
	v_mfma_f32_16x16x32_bf16 v[78:81], v[196:199], v[154:157], v[78:81]
	v_mfma_f32_16x16x32_bf16 v[74:77], v[228:231], v[154:157], v[74:77]
	v_mfma_f32_16x16x32_bf16 v[70:73], v[196:199], v[146:149], v[70:73]
	v_mfma_f32_16x16x32_bf16 v[66:69], v[228:231], v[146:149], v[66:69]
	v_mfma_f32_16x16x32_bf16 v[110:113], v[224:227], v[174:177], v[110:113]
	v_mfma_f32_16x16x32_bf16 v[106:109], v[232:235], v[174:177], v[106:109]
	v_mfma_f32_16x16x32_bf16 v[94:97], v[224:227], v[166:169], v[94:97]
	v_mfma_f32_16x16x32_bf16 v[90:93], v[232:235], v[166:169], v[90:93]
	v_mfma_f32_16x16x32_bf16 v[78:81], v[224:227], v[158:161], v[78:81]
	v_mfma_f32_16x16x32_bf16 v[74:77], v[232:235], v[158:161], v[74:77]
	v_mfma_f32_16x16x32_bf16 v[70:73], v[224:227], v[150:153], v[70:73]
	v_mfma_f32_16x16x32_bf16 v[66:69], v[232:235], v[150:153], v[66:69]
	s_mov_b32 m0, s17
	s_barrier
	ds_read_b128 v[146:149], v194 offset:16384
	ds_read_b128 v[150:153], v194 offset:17408
	ds_read_b128 v[154:157], v194 offset:18432
	ds_read_b128 v[158:161], v194 offset:19456
	ds_read_b128 v[162:165], v194 offset:20480
	ds_read_b128 v[166:169], v194 offset:21504
	ds_read_b128 v[170:173], v194 offset:22528
	ds_read_b128 v[174:177], v194 offset:23552
	global_load_lds_dwordx4 v0, s[34:35]
	s_mov_b32 m0, s46
	v_mov_b32_e32 v185, v1
	global_load_lds_dwordx4 v184, s[34:35]
	s_barrier
	s_waitcnt lgkmcnt(0)
	v_lshl_add_u64 v[206:207], s[34:35], 0, v[0:1]
	v_lshl_add_u64 v[208:209], s[34:35], 0, v[184:185]
	s_waitcnt lgkmcnt(0)
	v_mfma_f32_16x16x32_bf16 v[62:65], v[130:133], v[146:149], v[62:65]
	v_mfma_f32_16x16x32_bf16 v[58:61], v[138:141], v[146:149], v[58:61]
	v_mfma_f32_16x16x32_bf16 v[46:49], v[130:133], v[154:157], v[46:49]
	v_mfma_f32_16x16x32_bf16 v[42:45], v[138:141], v[154:157], v[42:45]
	v_mfma_f32_16x16x32_bf16 v[30:33], v[130:133], v[162:165], v[30:33]
	v_mfma_f32_16x16x32_bf16 v[26:29], v[138:141], v[162:165], v[26:29]
	v_mfma_f32_16x16x32_bf16 v[14:17], v[130:133], v[170:173], v[14:17]
	v_mfma_f32_16x16x32_bf16 v[10:13], v[138:141], v[170:173], v[10:13]
	v_mfma_f32_16x16x32_bf16 v[62:65], v[134:137], v[150:153], v[62:65]
	v_mfma_f32_16x16x32_bf16 v[58:61], v[142:145], v[150:153], v[58:61]
	v_mfma_f32_16x16x32_bf16 v[46:49], v[134:137], v[158:161], v[46:49]
	v_mfma_f32_16x16x32_bf16 v[42:45], v[142:145], v[158:161], v[42:45]
	v_mfma_f32_16x16x32_bf16 v[30:33], v[134:137], v[166:169], v[30:33]
	v_mfma_f32_16x16x32_bf16 v[26:29], v[142:145], v[166:169], v[26:29]
	v_mfma_f32_16x16x32_bf16 v[14:17], v[134:137], v[174:177], v[14:17]
	v_mfma_f32_16x16x32_bf16 v[10:13], v[142:145], v[174:177], v[10:13]
	s_barrier
	s_add_u32 s30, s4, 0x40000
	s_addc_u32 s31, s5, 0
	s_add_i32 s62, s64, s40
	v_lshl_add_u64 v[130:131], s[30:31], 0, v[178:179]
	s_mov_b32 m0, s62
	s_nop 0
	global_load_lds_dwordx4 v[130:131], off
	v_lshl_add_u64 v[130:131], s[30:31], 0, v[180:181]
	s_add_i32 m0, s62, 0x2000
	s_nop 0
	global_load_lds_dwordx4 v[130:131], off
	s_waitcnt vmcnt(6)
	s_barrier
	v_mfma_f32_16x16x32_bf16 v[54:57], v[196:199], v[146:149], v[54:57]
	v_mfma_f32_16x16x32_bf16 v[50:53], v[228:231], v[146:149], v[50:53]
	v_mfma_f32_16x16x32_bf16 v[38:41], v[196:199], v[154:157], v[38:41]
	v_mfma_f32_16x16x32_bf16 v[34:37], v[228:231], v[154:157], v[34:37]
	v_mfma_f32_16x16x32_bf16 v[22:25], v[196:199], v[162:165], v[22:25]
	v_mfma_f32_16x16x32_bf16 v[18:21], v[228:231], v[162:165], v[18:21]
	v_mfma_f32_16x16x32_bf16 v[6:9], v[196:199], v[170:173], v[6:9]
	v_mfma_f32_16x16x32_bf16 v[2:5], v[228:231], v[170:173], v[2:5]
	v_mfma_f32_16x16x32_bf16 v[54:57], v[224:227], v[150:153], v[54:57]
	v_mfma_f32_16x16x32_bf16 v[50:53], v[232:235], v[150:153], v[50:53]
	v_mfma_f32_16x16x32_bf16 v[38:41], v[224:227], v[158:161], v[38:41]
	v_mfma_f32_16x16x32_bf16 v[34:37], v[232:235], v[158:161], v[34:37]
	v_mfma_f32_16x16x32_bf16 v[22:25], v[224:227], v[166:169], v[22:25]
	v_mfma_f32_16x16x32_bf16 v[18:21], v[232:235], v[166:169], v[18:21]
	v_mfma_f32_16x16x32_bf16 v[6:9], v[224:227], v[174:177], v[6:9]
	v_mfma_f32_16x16x32_bf16 v[2:5], v[232:235], v[174:177], v[2:5]
	s_add_i32 s30, 0, 0x18000
	v_add_u32_e32 v142, s30, v192
	s_barrier
	ds_read_b128 v[130:133], v142
	ds_read_b128 v[134:137], v142 offset:1024
	ds_read_b128 v[138:141], v142 offset:2048
	ds_read_b128 v[142:145], v142 offset:3072
	s_mov_b32 m0, s47
	v_lshl_add_u64 v[188:189], s[34:35], 0, v[188:189]
	ds_read_b128 v[146:149], v194 offset:32768
	ds_read_b128 v[150:153], v194 offset:33792
	ds_read_b128 v[154:157], v194 offset:34816
	ds_read_b128 v[158:161], v194 offset:35840
	ds_read_b128 v[162:165], v194 offset:36864
	ds_read_b128 v[166:169], v194 offset:37888
	ds_read_b128 v[170:173], v194 offset:38912
	ds_read_b128 v[174:177], v194 offset:39936
	global_load_lds_dwordx4 v[188:189], off
	v_lshl_add_u64 v[188:189], s[34:35], 0, v[186:187]
	s_mov_b32 m0, s48
	s_nop 0
	global_load_lds_dwordx4 v[188:189], off
	s_waitcnt lgkmcnt(8)
	s_barrier
; #define PG8_STAGE(bufoff, gbase, voff) do { _Pragma("unroll") for (int _i = 0; _i < 2; ++_i) \
;         __builtin_amdgcn_global_load_lds((const unsigned*)((const char*)(gbase) + (voff)[_i]), (LAS unsigned*)(lds + (bufoff) + ldsw + _i * 8192), 16, 0, 0); } while (0)
; #define PG8_LDA(dst, b, h) do { _Pragma("unroll") for (int m = 0; m < 4; ++m) _Pragma("unroll") for (int k = 0; k < 2; ++k) dst[m][k] = *(const LAS bf16x8*)(lds + PG8_SA(b, h) + aoff + m * 2048 + k * 1024); } while (0)
; #define PG8_LDB(dst, b, h) do { _Pragma("unroll") for (int n = 0; n < 2; ++n) _Pragma("unroll") for (int k = 0; k < 2; ++k) dst[n][k] = *(const LAS bf16x8*)(lds + PG8_SB(b, h) + boff + n * 2048 + k * 1024); } while (0)
; #define PG8_MMA(ai, bj, At, Bt) do { __builtin_amdgcn_s_setprio(1); _Pragma("unroll") for (int m = 0; m < 4; ++m) _Pragma("unroll") for (int n = 0; n < 2; ++n) _Pragma("unroll") for (int k = 0; k < 2; ++k) \
;         acc[ai][bj][m][n] = __builtin_amdgcn_mfma_f32_16x16x32_bf16(Bt[n][k], At[m][k], acc[ai][bj][m][n], 0, 0, 0); __builtin_amdgcn_s_setprio(0); } while (0)
; #define PG8_WAIT_V(n) asm volatile("s_waitcnt vmcnt(" #n ")" ::: "memory")
; #define PG8_WAIT_L(n) asm volatile("s_waitcnt lgkmcnt(" #n ")" ::: "memory")
; #define PG8_BAR __builtin_amdgcn_s_barrier()
; #define PG8_SCHED __builtin_amdgcn_sched_barrier(0)
; template <class Epi, class Sched>
; __device__ __forceinline__ void gemm_phase(LAS unsigned char* lds, const bf16_t* Abase, const int K, const Sched& S, const Epi& E, const int wvid) {
;     ...
;             PG8_WAIT_L(8); PG8_BAR; PG8_WAIT_L(0); PG8_MMA(0, 0, At, B0); PG8_BAR; PG8_SCHED;
;             PG8_LDB(B1, 1, 1); PG8_STAGE(PG8_SB(1, 0), b3, voffB);
;             PG8_BAR; PG8_WAIT_L(0); PG8_MMA(0, 1, At, B1); PG8_BAR;
;             PG8_LDA(At, 1, 1); PG8_STAGE(PG8_SA(1, 0), a3, voffA[0]);
;             PG8_BAR; PG8_WAIT_L(0); PG8_MMA(1, 0, At, B0); PG8_BAR; PG8_SCHED;
;             PG8_STAGE(PG8_SB(1, 1), b3 + hstep, voffB);
;             PG8_WAIT_V(6); PG8_BAR; PG8_MMA(1, 1, At, B1); PG8_BAR;
;         }
	s_waitcnt lgkmcnt(0)
	s_waitcnt lgkmcnt(0)
	v_mfma_f32_16x16x32_bf16 v[126:129], v[130:133], v[146:149], v[126:129]
	v_mfma_f32_16x16x32_bf16 v[122:125], v[138:141], v[146:149], v[122:125]
	v_mfma_f32_16x16x32_bf16 v[118:121], v[130:133], v[154:157], v[118:121]
	v_mfma_f32_16x16x32_bf16 v[114:117], v[138:141], v[154:157], v[114:117]
	v_mfma_f32_16x16x32_bf16 v[102:105], v[130:133], v[162:165], v[102:105]
	v_mfma_f32_16x16x32_bf16 v[98:101], v[138:141], v[162:165], v[98:101]
	v_mfma_f32_16x16x32_bf16 v[86:89], v[130:133], v[170:173], v[86:89]
	v_mfma_f32_16x16x32_bf16 v[82:85], v[138:141], v[170:173], v[82:85]
	v_mfma_f32_16x16x32_bf16 v[126:129], v[134:137], v[150:153], v[126:129]
	v_mfma_f32_16x16x32_bf16 v[122:125], v[142:145], v[150:153], v[122:125]
	v_mfma_f32_16x16x32_bf16 v[118:121], v[134:137], v[158:161], v[118:121]
	v_mfma_f32_16x16x32_bf16 v[114:117], v[142:145], v[158:161], v[114:117]
	v_mfma_f32_16x16x32_bf16 v[102:105], v[134:137], v[166:169], v[102:105]
	v_mfma_f32_16x16x32_bf16 v[98:101], v[142:145], v[166:169], v[98:101]
	v_mfma_f32_16x16x32_bf16 v[86:89], v[134:137], v[174:177], v[86:89]
	v_mfma_f32_16x16x32_bf16 v[82:85], v[142:145], v[174:177], v[82:85]
	s_barrier
	s_add_i32 s31, 0, 0x1c000
	s_add_i32 s30, s30, s40
	v_add_u32_e32 v183, s31, v192
	v_lshl_add_u64 v[188:189], v[200:201], 0, s[12:13]
	s_mov_b32 m0, s30
	ds_read_b128 v[196:199], v183
	ds_read_b128 v[224:227], v183 offset:1024
	ds_read_b128 v[228:231], v183 offset:2048
	ds_read_b128 v[232:235], v183 offset:3072
	global_load_lds_dwordx4 v[188:189], off
	v_lshl_add_u64 v[188:189], v[202:203], 0, s[12:13]
	s_add_i32 m0, s30, 0x2000
	s_nop 0
	global_load_lds_dwordx4 v[188:189], off
	s_barrier
	s_waitcnt lgkmcnt(0)
	s_waitcnt lgkmcnt(0)
	v_mfma_f32_16x16x32_bf16 v[110:113], v[196:199], v[146:149], v[110:113]
	v_mfma_f32_16x16x32_bf16 v[106:109], v[228:231], v[146:149], v[106:109]
	v_mfma_f32_16x16x32_bf16 v[94:97], v[196:199], v[154:157], v[94:97]
	v_mfma_f32_16x16x32_bf16 v[90:93], v[228:231], v[154:157], v[90:93]
	v_mfma_f32_16x16x32_bf16 v[78:81], v[196:199], v[162:165], v[78:81]
	v_mfma_f32_16x16x32_bf16 v[74:77], v[228:231], v[162:165], v[74:77]
	v_mfma_f32_16x16x32_bf16 v[70:73], v[196:199], v[170:173], v[70:73]
	v_mfma_f32_16x16x32_bf16 v[66:69], v[228:231], v[170:173], v[66:69]
	v_mfma_f32_16x16x32_bf16 v[110:113], v[224:227], v[150:153], v[110:113]
	v_mfma_f32_16x16x32_bf16 v[106:109], v[232:235], v[150:153], v[106:109]
	v_mfma_f32_16x16x32_bf16 v[94:97], v[224:227], v[158:161], v[94:97]
	v_mfma_f32_16x16x32_bf16 v[90:93], v[232:235], v[158:161], v[90:93]
	v_mfma_f32_16x16x32_bf16 v[78:81], v[224:227], v[166:169], v[78:81]
	v_mfma_f32_16x16x32_bf16 v[74:77], v[232:235], v[166:169], v[74:77]
	v_mfma_f32_16x16x32_bf16 v[70:73], v[224:227], v[174:177], v[70:73]
	v_mfma_f32_16x16x32_bf16 v[66:69], v[232:235], v[174:177], v[66:69]
	s_mov_b32 m0, s52
	v_lshl_add_u64 v[188:189], v[206:207], 0, s[12:13]
	s_barrier
	ds_read_b128 v[146:149], v194 offset:49152
	ds_read_b128 v[150:153], v194 offset:50176
	ds_read_b128 v[154:157], v194 offset:51200
	ds_read_b128 v[158:161], v194 offset:52224
	ds_read_b128 v[162:165], v194 offset:53248
	ds_read_b128 v[166:169], v194 offset:54272
	ds_read_b128 v[170:173], v194 offset:55296
	ds_read_b128 v[174:177], v194 offset:56320
	global_load_lds_dwordx4 v[188:189], off
	v_lshl_add_u64 v[188:189], v[208:209], 0, s[12:13]
	s_mov_b32 m0, s53
	s_nop 0
	global_load_lds_dwordx4 v[188:189], off
	s_barrier
	s_waitcnt lgkmcnt(0)
	s_waitcnt lgkmcnt(0)
	v_mfma_f32_16x16x32_bf16 v[62:65], v[130:133], v[146:149], v[62:65]
	v_mfma_f32_16x16x32_bf16 v[58:61], v[138:141], v[146:149], v[58:61]
	v_mfma_f32_16x16x32_bf16 v[46:49], v[130:133], v[154:157], v[46:49]
	v_mfma_f32_16x16x32_bf16 v[42:45], v[138:141], v[154:157], v[42:45]
	v_mfma_f32_16x16x32_bf16 v[30:33], v[130:133], v[162:165], v[30:33]
	v_mfma_f32_16x16x32_bf16 v[26:29], v[138:141], v[162:165], v[26:29]
	v_mfma_f32_16x16x32_bf16 v[14:17], v[130:133], v[170:173], v[14:17]
	v_mfma_f32_16x16x32_bf16 v[10:13], v[138:141], v[170:173], v[10:13]
	v_mfma_f32_16x16x32_bf16 v[62:65], v[134:137], v[150:153], v[62:65]
	v_mfma_f32_16x16x32_bf16 v[58:61], v[142:145], v[150:153], v[58:61]
	v_mfma_f32_16x16x32_bf16 v[46:49], v[134:137], v[158:161], v[46:49]
	v_mfma_f32_16x16x32_bf16 v[42:45], v[142:145], v[158:161], v[42:45]
	v_mfma_f32_16x16x32_bf16 v[30:33], v[134:137], v[166:169], v[30:33]
	v_mfma_f32_16x16x32_bf16 v[26:29], v[142:145], v[166:169], v[26:29]
	v_mfma_f32_16x16x32_bf16 v[14:17], v[134:137], v[174:177], v[14:17]
	v_mfma_f32_16x16x32_bf16 v[10:13], v[142:145], v[174:177], v[10:13]
	s_barrier
	s_add_u32 s4, s4, 0x40080
	s_addc_u32 s5, s5, 0
	s_add_i32 s30, s31, s40
	v_lshl_add_u64 v[130:131], s[4:5], 0, v[178:179]
	s_mov_b32 m0, s30
	s_nop 0
	global_load_lds_dwordx4 v[130:131], off
	v_lshl_add_u64 v[130:131], s[4:5], 0, v[180:181]
	s_add_i32 m0, s30, 0x2000
	s_nop 0
	global_load_lds_dwordx4 v[130:131], off
	s_waitcnt vmcnt(6)
	s_barrier
	v_mfma_f32_16x16x32_bf16 v[54:57], v[196:199], v[146:149], v[54:57]
	v_mfma_f32_16x16x32_bf16 v[50:53], v[228:231], v[146:149], v[50:53]
	v_mfma_f32_16x16x32_bf16 v[38:41], v[196:199], v[154:157], v[38:41]
	v_mfma_f32_16x16x32_bf16 v[34:37], v[228:231], v[154:157], v[34:37]
	v_mfma_f32_16x16x32_bf16 v[22:25], v[196:199], v[162:165], v[22:25]
	v_mfma_f32_16x16x32_bf16 v[18:21], v[228:231], v[162:165], v[18:21]
	v_mfma_f32_16x16x32_bf16 v[6:9], v[196:199], v[170:173], v[6:9]
	v_mfma_f32_16x16x32_bf16 v[2:5], v[228:231], v[170:173], v[2:5]
	v_mfma_f32_16x16x32_bf16 v[54:57], v[224:227], v[150:153], v[54:57]
	v_mfma_f32_16x16x32_bf16 v[50:53], v[232:235], v[150:153], v[50:53]
	v_mfma_f32_16x16x32_bf16 v[38:41], v[224:227], v[158:161], v[38:41]
	v_mfma_f32_16x16x32_bf16 v[34:37], v[232:235], v[158:161], v[34:37]
	v_mfma_f32_16x16x32_bf16 v[22:25], v[224:227], v[166:169], v[22:25]
	v_mfma_f32_16x16x32_bf16 v[18:21], v[232:235], v[166:169], v[18:21]
	v_mfma_f32_16x16x32_bf16 v[6:9], v[224:227], v[174:177], v[6:9]
	v_mfma_f32_16x16x32_bf16 v[2:5], v[232:235], v[174:177], v[2:5]
	s_add_i32 s61, s61, 2
	s_cmp_gt_u32 s61, 13
	s_barrier
	s_cbranch_scc1 .LBB0_130
	s_mov_b64 s[4:5], s[28:29]
	s_branch .LBB0_125

; #define PG8_STAGE(bufoff, gbase, voff) do { _Pragma("unroll") for (int _i = 0; _i < 2; ++_i) \
;         __builtin_amdgcn_global_load_lds((const unsigned*)((const char*)(gbase) + (voff)[_i]), (LAS unsigned*)(lds + (bufoff) + ldsw + _i * 8192), 16, 0, 0); } while (0)
; #define PG8_LDA(dst, b, h) do { _Pragma("unroll") for (int m = 0; m < 4; ++m) _Pragma("unroll") for (int k = 0; k < 2; ++k) dst[m][k] = *(const LAS bf16x8*)(lds + PG8_SA(b, h) + aoff + m * 2048 + k * 1024); } while (0)
; #define PG8_LDB(dst, b, h) do { _Pragma("unroll") for (int n = 0; n < 2; ++n) _Pragma("unroll") for (int k = 0; k < 2; ++k) dst[n][k] = *(const LAS bf16x8*)(lds + PG8_SB(b, h) + boff + n * 2048 + k * 1024); } while (0)
; #define PG8_MMA(ai, bj, At, Bt) do { __builtin_amdgcn_s_setprio(1); _Pragma("unroll") for (int m = 0; m < 4; ++m) _Pragma("unroll") for (int n = 0; n < 2; ++n) _Pragma("unroll") for (int k = 0; k < 2; ++k) \
;         acc[ai][bj][m][n] = __builtin_amdgcn_mfma_f32_16x16x32_bf16(Bt[n][k], At[m][k], acc[ai][bj][m][n], 0, 0, 0); __builtin_amdgcn_s_setprio(0); } while (0)
; #define PG8_WAIT_L(n) asm volatile("s_waitcnt lgkmcnt(" #n ")" ::: "memory")
; #define PG8_BAR __builtin_amdgcn_s_barrier()
; #define PG8_SCHED __builtin_amdgcn_sched_barrier(0)
; #define PG8_AOFF(u) do { const int _t = lt_tid(wvid); _Pragma("unroll") for (int _i = 0; _i < 2; ++_i) { int _R, _C; stage_rc(_t * 16 + _i * 8192, _R, _C); \
;         _Pragma("unroll") for (int _h = 0; _h < 2; ++_h) voffA[_h][_i] = (S.a_row(u, _h * HALF + _R) * (unsigned)K + (unsigned)(_C + (u).koff)) * 2u; } } while (0)
; template <class Epi, class Sched>
; __device__ __forceinline__ void gemm_phase(LAS unsigned char* lds, const bf16_t* Abase, const int K, const Sched& S, const Epi& E, const int wvid) {
;     ...
;             PG8_LDB(B0, 0, 0); PG8_SCHED; PG8_LDA(At, 0, 0); PG8_STAGE(PG8_SA(1, 1), a1, voffA[1]);
;             PG8_WAIT_L(8); PG8_BAR; PG8_WAIT_L(0); PG8_MMA(0, 0, At, B0); PG8_BAR; PG8_SCHED;
;             if (last && has_next) PG8_AOFF(nxt);
.LBB0_1002:
	v_add_u32_e32 v130, 0, v194
	v_add_u32_e32 v142, 0x10000, v130
	ds_read_b128 v[130:133], v142
	ds_read_b128 v[134:137], v142 offset:1024
	ds_read_b128 v[138:141], v142 offset:2048
	ds_read_b128 v[142:145], v142 offset:3072
	s_cmp_eq_u32 s59, s60
	s_cselect_b64 s[30:31], -1, 0
	s_add_i32 m0, s42, 0xc000
	s_add_u32 s28, s6, s26
	s_addc_u32 s29, s7, s27
	ds_read_b128 v[170:173], v195
	ds_read_b128 v[174:177], v195 offset:1024
	ds_read_b128 v[162:165], v195 offset:2048
	ds_read_b128 v[166:169], v195 offset:3072
	ds_read_b128 v[154:157], v195 offset:4096
	ds_read_b128 v[158:161], v195 offset:5120
	ds_read_b128 v[146:149], v195 offset:6144
	ds_read_b128 v[150:153], v195 offset:7168
	global_load_lds_dwordx4 v182, s[28:29]
	s_add_i32 m0, s42, 0xe000
	s_nop 0
	global_load_lds_dwordx4 v186, s[28:29]
	s_waitcnt lgkmcnt(8)
	s_barrier
	s_waitcnt lgkmcnt(0)
	s_waitcnt lgkmcnt(0)
	v_mfma_f32_16x16x32_bf16 v[126:129], v[130:133], v[170:173], v[126:129]
	v_mfma_f32_16x16x32_bf16 v[122:125], v[138:141], v[170:173], v[122:125]
	v_mfma_f32_16x16x32_bf16 v[118:121], v[130:133], v[162:165], v[118:121]
	v_mfma_f32_16x16x32_bf16 v[114:117], v[138:141], v[162:165], v[114:117]
	v_mfma_f32_16x16x32_bf16 v[110:113], v[130:133], v[154:157], v[110:113]
	v_mfma_f32_16x16x32_bf16 v[106:109], v[138:141], v[154:157], v[106:109]
	v_mfma_f32_16x16x32_bf16 v[102:105], v[130:133], v[146:149], v[102:105]
	v_mfma_f32_16x16x32_bf16 v[98:101], v[138:141], v[146:149], v[98:101]
	v_mfma_f32_16x16x32_bf16 v[126:129], v[134:137], v[174:177], v[126:129]
	v_mfma_f32_16x16x32_bf16 v[122:125], v[142:145], v[174:177], v[122:125]
	v_mfma_f32_16x16x32_bf16 v[118:121], v[134:137], v[166:169], v[118:121]
	v_mfma_f32_16x16x32_bf16 v[114:117], v[142:145], v[166:169], v[114:117]
	v_mfma_f32_16x16x32_bf16 v[110:113], v[134:137], v[158:161], v[110:113]
	v_mfma_f32_16x16x32_bf16 v[106:109], v[142:145], v[158:161], v[106:109]
	v_mfma_f32_16x16x32_bf16 v[102:105], v[134:137], v[150:153], v[102:105]
	v_mfma_f32_16x16x32_bf16 v[98:101], v[142:145], v[150:153], v[98:101]
	s_barrier
	s_and_b64 s[28:29], s[24:25], s[30:31]
	s_andn2_b64 vcc, exec, s[28:29]
	s_cbranch_vccnz .LBB0_1004
	v_mbcnt_lo_u32_b32 v0, -1, 0
	v_mbcnt_hi_u32_b32 v0, -1, v0
	s_nop 0
	v_or_b32_e32 v0, s75, v0
	v_ashrrev_i32_e32 v183, 31, v0
	v_lshrrev_b32_e32 v183, 26, v183
	v_lshlrev_b32_e32 v182, 4, v0
	v_add_u32_e32 v183, v0, v183
	v_bfe_i32 v0, v0, 27, 1
	v_lshrrev_b32_e32 v0, 22, v0
	v_add_u32_e32 v0, v182, v0
	v_and_b32_e32 v0, 0xfffffc00, v0
	v_sub_u32_e32 v0, v182, v0
	v_lshrrev_b32_e32 v184, 4, v0
	v_bitop3_b32 v0, v184, v0, 32 bitop3:0x6c
	v_ashrrev_i32_e32 v185, 31, v0
	v_lshrrev_b32_e32 v185, 26, v185
	v_add_u32_e32 v185, v0, v185
	v_ashrrev_i32_e32 v183, 6, v183
	v_lshrrev_b32_e32 v186, 6, v185
	v_and_b32_e32 v185, 0xc0, v185
	v_lshlrev_b32_e32 v184, 3, v183
	v_sub_u32_e32 v0, v0, v185
	v_and_b32_e32 v184, 0x1ffff0, v184
	v_lshlrev_b32_e32 v183, 5, v183
	v_ashrrev_i16_sdwa v0, v216, sext(v0) dst_sel:DWORD dst_unused:UNUSED_PAD src0_sel:DWORD src1_sel:BYTE_0
	v_and_b32_e32 v183, 32, v183
	v_bfe_i32 v0, v0, 0, 16
	v_add_u32_e32 v184, s55, v184
	v_add_u32_e32 v182, 0x2000, v182
	v_add3_u32 v0, v183, s16, v0
	v_add_lshl_u32 v183, v184, v186, 11
	v_ashrrev_i32_e32 v184, 31, v182
	v_lshrrev_b32_e32 v184, 22, v184
	v_add_u32_e32 v184, v182, v184
	v_ashrrev_i32_e32 v184, 10, v184
	v_mul_i32_i24_e32 v185, 0x400, v184
	v_sub_u32_e32 v182, v182, v185
	v_lshrrev_b32_e32 v185, 4, v182
	v_bitop3_b32 v182, v185, v182, 32 bitop3:0x6c
	v_ashrrev_i32_e32 v186, 31, v182
	v_lshrrev_b32_e32 v186, 26, v186
	v_add_u32_e32 v186, v182, v186
	v_lshrrev_b32_e32 v187, 6, v186
	v_and_b32_e32 v186, 0xc0, v186
	v_lshlrev_b32_e32 v185, 3, v184
	v_sub_u32_e32 v182, v182, v186
	v_and_b32_e32 v185, 0x1ffff0, v185
	v_lshlrev_b32_e32 v184, 5, v184
	v_ashrrev_i16_sdwa v182, v216, sext(v182) dst_sel:DWORD dst_unused:UNUSED_PAD src0_sel:DWORD src1_sel:BYTE_0
	v_and_b32_e32 v184, 32, v184
	v_bfe_i32 v182, v182, 0, 16
	v_add_u32_e32 v185, s55, v185
	v_lshl_add_u32 v183, v0, 1, v183
	v_add3_u32 v182, v184, s16, v182
	v_add_lshl_u32 v184, v185, v187, 11
	v_add_u32_e32 v0, 0x40000, v183
	v_lshl_add_u32 v184, v182, 1, v184
	v_add_u32_e32 v186, 0x40000, v184
	v_mov_b32_e32 v187, v1
	v_mov_b64_e32 v[192:193], v[0:1]
	v_mov_b32_e32 v182, v0
	v_mov_b32_e32 v0, v183
	s_branch .LBB0_1005

; #define PG8_STAGE(bufoff, gbase, voff) do { _Pragma("unroll") for (int _i = 0; _i < 2; ++_i) \
;         __builtin_amdgcn_global_load_lds((const unsigned*)((const char*)(gbase) + (voff)[_i]), (LAS unsigned*)(lds + (bufoff) + ldsw + _i * 8192), 16, 0, 0); } while (0)
; #define PG8_LDA(dst, b, h) do { _Pragma("unroll") for (int m = 0; m < 4; ++m) _Pragma("unroll") for (int k = 0; k < 2; ++k) dst[m][k] = *(const LAS bf16x8*)(lds + PG8_SA(b, h) + aoff + m * 2048 + k * 1024); } while (0)
; #define PG8_LDB(dst, b, h) do { _Pragma("unroll") for (int n = 0; n < 2; ++n) _Pragma("unroll") for (int k = 0; k < 2; ++k) dst[n][k] = *(const LAS bf16x8*)(lds + PG8_SB(b, h) + boff + n * 2048 + k * 1024); } while (0)
; #define PG8_MMA(ai, bj, At, Bt) do { __builtin_amdgcn_s_setprio(1); _Pragma("unroll") for (int m = 0; m < 4; ++m) _Pragma("unroll") for (int n = 0; n < 2; ++n) _Pragma("unroll") for (int k = 0; k < 2; ++k) \
;         acc[ai][bj][m][n] = __builtin_amdgcn_mfma_f32_16x16x32_bf16(Bt[n][k], At[m][k], acc[ai][bj][m][n], 0, 0, 0); __builtin_amdgcn_s_setprio(0); } while (0)
; #define PG8_WAIT_V(n) asm volatile("s_waitcnt vmcnt(" #n ")" ::: "memory")
; #define PG8_WAIT_L(n) asm volatile("s_waitcnt lgkmcnt(" #n ")" ::: "memory")
; #define PG8_BAR __builtin_amdgcn_s_barrier()
; #define PG8_SCHED __builtin_amdgcn_sched_barrier(0)
; template <class Epi, class Sched>
; __device__ __forceinline__ void gemm_phase(LAS unsigned char* lds, const bf16_t* Abase, const int K, const Sched& S, const Epi& E, const int wvid) {
;     ...
;             const char* a2 = last ? Ab : Ab + (size_t)(t + 2) * kstep; const char* b2 = last ? nB : cB + (size_t)(t + 2) * kstep;
;             const char* a3 = a2 + kstep; const char* b3 = b2 + kstep;
;             PG8_LDB(B1, 0, 1); PG8_STAGE(PG8_SB(0, 0), b2, voffB);
;             PG8_BAR; PG8_WAIT_L(0); PG8_MMA(0, 1, At, B1); PG8_BAR;
;             PG8_LDA(At, 0, 1); PG8_STAGE(PG8_SA(0, 0), a2, voffA[0]);
;             PG8_BAR; PG8_WAIT_L(0); PG8_MMA(1, 0, At, B0); PG8_BAR; PG8_SCHED;
;             PG8_STAGE(PG8_SB(0, 1), b2 + hstep, voffB);
;             PG8_WAIT_V(6); PG8_BAR; PG8_MMA(1, 1, At, B1); PG8_BAR;
;             PG8_LDB(B0, 1, 0); PG8_SCHED; PG8_LDA(At, 1, 0); PG8_STAGE(PG8_SA(0, 1), a2, voffA[1]);
.LBB0_1005:
	s_add_i32 s60, s60, 2
	s_add_u32 s28, s26, 0x100
	s_addc_u32 s29, s27, 0
	s_and_b64 s[34:35], s[30:31], exec
	s_cselect_b32 s34, 0, s28
	s_cselect_b32 s35, 0, s29
	s_add_u32 s34, s0, s34
	s_addc_u32 s35, s1, s35
	s_add_u32 s61, s23, s26
	s_addc_u32 s62, s58, s27
	s_add_i32 s63, 0, 0x14000
	s_and_b64 s[26:27], s[30:31], exec
	s_cselect_b32 s27, s11, s62
	s_cselect_b32 s26, s17, s61
	s_mov_b32 m0, s43
	v_add_u32_e32 v183, s63, v194
	v_lshl_add_u64 v[224:225], s[26:27], 0, v[178:179]
	ds_read_b128 v[196:199], v183
	ds_read_b128 v[200:203], v183 offset:1024
	ds_read_b128 v[206:209], v183 offset:2048
	ds_read_b128 v[210:213], v183 offset:3072
	global_load_lds_dwordx4 v[224:225], off
	v_lshl_add_u64 v[226:227], s[26:27], 0, v[180:181]
	s_mov_b32 m0, s46
	s_nop 0
	global_load_lds_dwordx4 v[226:227], off
	s_barrier
	s_waitcnt lgkmcnt(0)
	s_waitcnt lgkmcnt(0)
	v_mfma_f32_16x16x32_bf16 v[94:97], v[196:199], v[170:173], v[94:97]
	v_mfma_f32_16x16x32_bf16 v[90:93], v[206:209], v[170:173], v[90:93]
	v_mfma_f32_16x16x32_bf16 v[86:89], v[196:199], v[162:165], v[86:89]
	v_mfma_f32_16x16x32_bf16 v[82:85], v[206:209], v[162:165], v[82:85]
	v_mfma_f32_16x16x32_bf16 v[78:81], v[196:199], v[154:157], v[78:81]
	v_mfma_f32_16x16x32_bf16 v[74:77], v[206:209], v[154:157], v[74:77]
	v_mfma_f32_16x16x32_bf16 v[70:73], v[196:199], v[146:149], v[70:73]
	v_mfma_f32_16x16x32_bf16 v[66:69], v[206:209], v[146:149], v[66:69]
	v_mfma_f32_16x16x32_bf16 v[94:97], v[200:203], v[174:177], v[94:97]
	v_mfma_f32_16x16x32_bf16 v[90:93], v[210:213], v[174:177], v[90:93]
	v_mfma_f32_16x16x32_bf16 v[86:89], v[200:203], v[166:169], v[86:89]
	v_mfma_f32_16x16x32_bf16 v[82:85], v[210:213], v[166:169], v[82:85]
	v_mfma_f32_16x16x32_bf16 v[78:81], v[200:203], v[158:161], v[78:81]
	v_mfma_f32_16x16x32_bf16 v[74:77], v[210:213], v[158:161], v[74:77]
	v_mfma_f32_16x16x32_bf16 v[70:73], v[200:203], v[150:153], v[70:73]
	v_mfma_f32_16x16x32_bf16 v[66:69], v[210:213], v[150:153], v[66:69]
	s_mov_b32 m0, s42
	s_barrier
	ds_read_b128 v[146:149], v195 offset:16384
	ds_read_b128 v[150:153], v195 offset:17408
	ds_read_b128 v[154:157], v195 offset:18432
	ds_read_b128 v[158:161], v195 offset:19456
	ds_read_b128 v[162:165], v195 offset:20480
	ds_read_b128 v[166:169], v195 offset:21504
	ds_read_b128 v[170:173], v195 offset:22528
	ds_read_b128 v[174:177], v195 offset:23552
	global_load_lds_dwordx4 v0, s[34:35]
	s_mov_b32 m0, s47
	v_mov_b32_e32 v185, v1
	global_load_lds_dwordx4 v184, s[34:35]
	s_barrier
	s_waitcnt lgkmcnt(0)
	v_lshl_add_u64 v[228:229], s[34:35], 0, v[0:1]
	v_lshl_add_u64 v[230:231], s[34:35], 0, v[184:185]
	s_waitcnt lgkmcnt(0)
	v_mfma_f32_16x16x32_bf16 v[62:65], v[130:133], v[146:149], v[62:65]
	v_mfma_f32_16x16x32_bf16 v[58:61], v[138:141], v[146:149], v[58:61]
	v_mfma_f32_16x16x32_bf16 v[54:57], v[130:133], v[154:157], v[54:57]
	v_mfma_f32_16x16x32_bf16 v[50:53], v[138:141], v[154:157], v[50:53]
	v_mfma_f32_16x16x32_bf16 v[42:45], v[130:133], v[162:165], v[42:45]
	v_mfma_f32_16x16x32_bf16 v[34:37], v[138:141], v[162:165], v[34:37]
	v_mfma_f32_16x16x32_bf16 v[26:29], v[130:133], v[170:173], v[26:29]
	v_mfma_f32_16x16x32_bf16 v[18:21], v[138:141], v[170:173], v[18:21]
	v_mfma_f32_16x16x32_bf16 v[62:65], v[134:137], v[150:153], v[62:65]
	v_mfma_f32_16x16x32_bf16 v[58:61], v[142:145], v[150:153], v[58:61]
	v_mfma_f32_16x16x32_bf16 v[54:57], v[134:137], v[158:161], v[54:57]
	v_mfma_f32_16x16x32_bf16 v[50:53], v[142:145], v[158:161], v[50:53]
	v_mfma_f32_16x16x32_bf16 v[42:45], v[134:137], v[166:169], v[42:45]
	v_mfma_f32_16x16x32_bf16 v[34:37], v[142:145], v[166:169], v[34:37]
	v_mfma_f32_16x16x32_bf16 v[26:29], v[134:137], v[174:177], v[26:29]
	v_mfma_f32_16x16x32_bf16 v[18:21], v[142:145], v[174:177], v[18:21]
	s_barrier
	s_add_u32 s30, s26, 0x40000
	s_addc_u32 s31, s27, 0
	s_add_i32 s61, s63, s40
	v_lshl_add_u64 v[130:131], s[30:31], 0, v[178:179]
	s_mov_b32 m0, s61
	s_nop 0
	global_load_lds_dwordx4 v[130:131], off
	v_lshl_add_u64 v[130:131], s[30:31], 0, v[180:181]
	s_add_i32 m0, s61, 0x2000
	s_nop 0
	global_load_lds_dwordx4 v[130:131], off
	s_waitcnt vmcnt(6)
	s_barrier
	v_mfma_f32_16x16x32_bf16 v[46:49], v[196:199], v[146:149], v[46:49]
	v_mfma_f32_16x16x32_bf16 v[38:41], v[206:209], v[146:149], v[38:41]
	v_mfma_f32_16x16x32_bf16 v[30:33], v[196:199], v[154:157], v[30:33]
	v_mfma_f32_16x16x32_bf16 v[22:25], v[206:209], v[154:157], v[22:25]
	v_mfma_f32_16x16x32_bf16 v[14:17], v[196:199], v[162:165], v[14:17]
	v_mfma_f32_16x16x32_bf16 v[10:13], v[206:209], v[162:165], v[10:13]
	v_mfma_f32_16x16x32_bf16 v[6:9], v[196:199], v[170:173], v[6:9]
	v_mfma_f32_16x16x32_bf16 v[2:5], v[206:209], v[170:173], v[2:5]
	v_mfma_f32_16x16x32_bf16 v[46:49], v[200:203], v[150:153], v[46:49]
	v_mfma_f32_16x16x32_bf16 v[38:41], v[210:213], v[150:153], v[38:41]
	v_mfma_f32_16x16x32_bf16 v[30:33], v[200:203], v[158:161], v[30:33]
	v_mfma_f32_16x16x32_bf16 v[22:25], v[210:213], v[158:161], v[22:25]
	v_mfma_f32_16x16x32_bf16 v[14:17], v[200:203], v[166:169], v[14:17]
	v_mfma_f32_16x16x32_bf16 v[10:13], v[210:213], v[166:169], v[10:13]
	v_mfma_f32_16x16x32_bf16 v[6:9], v[200:203], v[174:177], v[6:9]
	v_mfma_f32_16x16x32_bf16 v[2:5], v[210:213], v[174:177], v[2:5]
	s_add_i32 s30, 0, 0x18000
	v_add_u32_e32 v142, s30, v194
	s_barrier
; #define PG8_STAGE(bufoff, gbase, voff) do { _Pragma("unroll") for (int _i = 0; _i < 2; ++_i) \
;         __builtin_amdgcn_global_load_lds((const unsigned*)((const char*)(gbase) + (voff)[_i]), (LAS unsigned*)(lds + (bufoff) + ldsw + _i * 8192), 16, 0, 0); } while (0)
; #define PG8_LDA(dst, b, h) do { _Pragma("unroll") for (int m = 0; m < 4; ++m) _Pragma("unroll") for (int k = 0; k < 2; ++k) dst[m][k] = *(const LAS bf16x8*)(lds + PG8_SA(b, h) + aoff + m * 2048 + k * 1024); } while (0)
; #define PG8_LDB(dst, b, h) do { _Pragma("unroll") for (int n = 0; n < 2; ++n) _Pragma("unroll") for (int k = 0; k < 2; ++k) dst[n][k] = *(const LAS bf16x8*)(lds + PG8_SB(b, h) + boff + n * 2048 + k * 1024); } while (0)
; #define PG8_MMA(ai, bj, At, Bt) do { __builtin_amdgcn_s_setprio(1); _Pragma("unroll") for (int m = 0; m < 4; ++m) _Pragma("unroll") for (int n = 0; n < 2; ++n) _Pragma("unroll") for (int k = 0; k < 2; ++k) \
;         acc[ai][bj][m][n] = __builtin_amdgcn_mfma_f32_16x16x32_bf16(Bt[n][k], At[m][k], acc[ai][bj][m][n], 0, 0, 0); __builtin_amdgcn_s_setprio(0); } while (0)
; #define PG8_WAIT_V(n) asm volatile("s_waitcnt vmcnt(" #n ")" ::: "memory")
; #define PG8_WAIT_L(n) asm volatile("s_waitcnt lgkmcnt(" #n ")" ::: "memory")
; #define PG8_BAR __builtin_amdgcn_s_barrier()
; #define PG8_SCHED __builtin_amdgcn_sched_barrier(0)
; template <class Epi, class Sched>
; __device__ __forceinline__ void gemm_phase(LAS unsigned char* lds, const bf16_t* Abase, const int K, const Sched& S, const Epi& E, const int wvid) {
;     ...
;             PG8_LDB(B0, 1, 0); PG8_SCHED; PG8_LDA(At, 1, 0); PG8_STAGE(PG8_SA(0, 1), a2, voffA[1]);
;             PG8_WAIT_L(8); PG8_BAR; PG8_WAIT_L(0); PG8_MMA(0, 0, At, B0); PG8_BAR; PG8_SCHED;
;             PG8_LDB(B1, 1, 1); PG8_STAGE(PG8_SB(1, 0), b3, voffB);
;             PG8_BAR; PG8_WAIT_L(0); PG8_MMA(0, 1, At, B1); PG8_BAR;
;             PG8_LDA(At, 1, 1); PG8_STAGE(PG8_SA(1, 0), a3, voffA[0]);
;             PG8_BAR; PG8_WAIT_L(0); PG8_MMA(1, 0, At, B0); PG8_BAR; PG8_SCHED;
;             PG8_STAGE(PG8_SB(1, 1), b3 + hstep, voffB);
;             PG8_WAIT_V(6); PG8_BAR; PG8_MMA(1, 1, At, B1); PG8_BAR;
;         }
	ds_read_b128 v[130:133], v142
	ds_read_b128 v[134:137], v142 offset:1024
	ds_read_b128 v[138:141], v142 offset:2048
	ds_read_b128 v[142:145], v142 offset:3072
	s_mov_b32 m0, s48
	v_lshl_add_u64 v[192:193], s[34:35], 0, v[192:193]
	ds_read_b128 v[146:149], v195 offset:32768
	ds_read_b128 v[150:153], v195 offset:33792
	ds_read_b128 v[154:157], v195 offset:34816
	ds_read_b128 v[158:161], v195 offset:35840
	ds_read_b128 v[162:165], v195 offset:36864
	ds_read_b128 v[166:169], v195 offset:37888
	ds_read_b128 v[170:173], v195 offset:38912
	ds_read_b128 v[174:177], v195 offset:39936
	global_load_lds_dwordx4 v[192:193], off
	v_lshl_add_u64 v[192:193], s[34:35], 0, v[186:187]
	s_mov_b32 m0, s49
	s_nop 0
	global_load_lds_dwordx4 v[192:193], off
	s_waitcnt lgkmcnt(8)
	s_barrier
	s_waitcnt lgkmcnt(0)
	s_waitcnt lgkmcnt(0)
	v_mfma_f32_16x16x32_bf16 v[126:129], v[130:133], v[146:149], v[126:129]
	v_mfma_f32_16x16x32_bf16 v[122:125], v[138:141], v[146:149], v[122:125]
	v_mfma_f32_16x16x32_bf16 v[118:121], v[130:133], v[154:157], v[118:121]
	v_mfma_f32_16x16x32_bf16 v[114:117], v[138:141], v[154:157], v[114:117]
	v_mfma_f32_16x16x32_bf16 v[110:113], v[130:133], v[162:165], v[110:113]
	v_mfma_f32_16x16x32_bf16 v[106:109], v[138:141], v[162:165], v[106:109]
	v_mfma_f32_16x16x32_bf16 v[102:105], v[130:133], v[170:173], v[102:105]
	v_mfma_f32_16x16x32_bf16 v[98:101], v[138:141], v[170:173], v[98:101]
	v_mfma_f32_16x16x32_bf16 v[126:129], v[134:137], v[150:153], v[126:129]
	v_mfma_f32_16x16x32_bf16 v[122:125], v[142:145], v[150:153], v[122:125]
	v_mfma_f32_16x16x32_bf16 v[118:121], v[134:137], v[158:161], v[118:121]
	v_mfma_f32_16x16x32_bf16 v[114:117], v[142:145], v[158:161], v[114:117]
	v_mfma_f32_16x16x32_bf16 v[110:113], v[134:137], v[166:169], v[110:113]
	v_mfma_f32_16x16x32_bf16 v[106:109], v[142:145], v[166:169], v[106:109]
	v_mfma_f32_16x16x32_bf16 v[102:105], v[134:137], v[174:177], v[102:105]
	v_mfma_f32_16x16x32_bf16 v[98:101], v[142:145], v[174:177], v[98:101]
	s_barrier
	s_add_i32 s31, 0, 0x1c000
	s_add_i32 s30, s30, s40
	v_add_u32_e32 v183, s31, v194
	v_lshl_add_u64 v[192:193], v[224:225], 0, s[12:13]
	s_mov_b32 m0, s30
	ds_read_b128 v[196:199], v183
	ds_read_b128 v[200:203], v183 offset:1024
	ds_read_b128 v[206:209], v183 offset:2048
	ds_read_b128 v[210:213], v183 offset:3072
	global_load_lds_dwordx4 v[192:193], off
	v_lshl_add_u64 v[192:193], v[226:227], 0, s[12:13]
	s_add_i32 m0, s30, 0x2000
	s_nop 0
	global_load_lds_dwordx4 v[192:193], off
	s_barrier
	s_waitcnt lgkmcnt(0)
	s_waitcnt lgkmcnt(0)
	v_mfma_f32_16x16x32_bf16 v[94:97], v[196:199], v[146:149], v[94:97]
	v_mfma_f32_16x16x32_bf16 v[90:93], v[206:209], v[146:149], v[90:93]
	v_mfma_f32_16x16x32_bf16 v[86:89], v[196:199], v[154:157], v[86:89]
	v_mfma_f32_16x16x32_bf16 v[82:85], v[206:209], v[154:157], v[82:85]
	v_mfma_f32_16x16x32_bf16 v[78:81], v[196:199], v[162:165], v[78:81]
	v_mfma_f32_16x16x32_bf16 v[74:77], v[206:209], v[162:165], v[74:77]
	v_mfma_f32_16x16x32_bf16 v[70:73], v[196:199], v[170:173], v[70:73]
	v_mfma_f32_16x16x32_bf16 v[66:69], v[206:209], v[170:173], v[66:69]
	v_mfma_f32_16x16x32_bf16 v[94:97], v[200:203], v[150:153], v[94:97]
	v_mfma_f32_16x16x32_bf16 v[90:93], v[210:213], v[150:153], v[90:93]
	v_mfma_f32_16x16x32_bf16 v[86:89], v[200:203], v[158:161], v[86:89]
	v_mfma_f32_16x16x32_bf16 v[82:85], v[210:213], v[158:161], v[82:85]
	v_mfma_f32_16x16x32_bf16 v[78:81], v[200:203], v[166:169], v[78:81]
	v_mfma_f32_16x16x32_bf16 v[74:77], v[210:213], v[166:169], v[74:77]
	v_mfma_f32_16x16x32_bf16 v[70:73], v[200:203], v[174:177], v[70:73]
	v_mfma_f32_16x16x32_bf16 v[66:69], v[210:213], v[174:177], v[66:69]
	s_mov_b32 m0, s51
	v_lshl_add_u64 v[192:193], v[228:229], 0, s[12:13]
	s_barrier
	ds_read_b128 v[146:149], v195 offset:49152
	ds_read_b128 v[150:153], v195 offset:50176
	ds_read_b128 v[154:157], v195 offset:51200
	ds_read_b128 v[158:161], v195 offset:52224
	ds_read_b128 v[162:165], v195 offset:53248
	ds_read_b128 v[166:169], v195 offset:54272
	ds_read_b128 v[170:173], v195 offset:55296
	ds_read_b128 v[174:177], v195 offset:56320
	global_load_lds_dwordx4 v[192:193], off
	v_lshl_add_u64 v[192:193], v[230:231], 0, s[12:13]
	s_mov_b32 m0, s52
	s_nop 0
	global_load_lds_dwordx4 v[192:193], off
	s_barrier
	s_waitcnt lgkmcnt(0)
	s_waitcnt lgkmcnt(0)
	v_mfma_f32_16x16x32_bf16 v[62:65], v[130:133], v[146:149], v[62:65]
	v_mfma_f32_16x16x32_bf16 v[58:61], v[138:141], v[146:149], v[58:61]
	v_mfma_f32_16x16x32_bf16 v[54:57], v[130:133], v[154:157], v[54:57]
	v_mfma_f32_16x16x32_bf16 v[50:53], v[138:141], v[154:157], v[50:53]
	v_mfma_f32_16x16x32_bf16 v[42:45], v[130:133], v[162:165], v[42:45]
	v_mfma_f32_16x16x32_bf16 v[34:37], v[138:141], v[162:165], v[34:37]
	v_mfma_f32_16x16x32_bf16 v[26:29], v[130:133], v[170:173], v[26:29]
	v_mfma_f32_16x16x32_bf16 v[18:21], v[138:141], v[170:173], v[18:21]
	v_mfma_f32_16x16x32_bf16 v[62:65], v[134:137], v[150:153], v[62:65]
	v_mfma_f32_16x16x32_bf16 v[58:61], v[142:145], v[150:153], v[58:61]
	v_mfma_f32_16x16x32_bf16 v[54:57], v[134:137], v[158:161], v[54:57]
	v_mfma_f32_16x16x32_bf16 v[50:53], v[142:145], v[158:161], v[50:53]
	v_mfma_f32_16x16x32_bf16 v[42:45], v[134:137], v[166:169], v[42:45]
	v_mfma_f32_16x16x32_bf16 v[34:37], v[142:145], v[166:169], v[34:37]
	v_mfma_f32_16x16x32_bf16 v[26:29], v[134:137], v[174:177], v[26:29]
	v_mfma_f32_16x16x32_bf16 v[18:21], v[142:145], v[174:177], v[18:21]
	s_barrier
	s_add_u32 s26, s26, 0x40080
	s_addc_u32 s27, s27, 0
	s_add_i32 s30, s31, s40
	v_lshl_add_u64 v[130:131], s[26:27], 0, v[178:179]
	s_mov_b32 m0, s30
	s_nop 0
	global_load_lds_dwordx4 v[130:131], off
	v_lshl_add_u64 v[130:131], s[26:27], 0, v[180:181]
	s_add_i32 m0, s30, 0x2000
	s_nop 0
	global_load_lds_dwordx4 v[130:131], off
	s_waitcnt vmcnt(6)
	s_barrier
	v_mfma_f32_16x16x32_bf16 v[46:49], v[196:199], v[146:149], v[46:49]
	v_mfma_f32_16x16x32_bf16 v[38:41], v[206:209], v[146:149], v[38:41]
	v_mfma_f32_16x16x32_bf16 v[30:33], v[196:199], v[154:157], v[30:33]
	v_mfma_f32_16x16x32_bf16 v[22:25], v[206:209], v[154:157], v[22:25]
	v_mfma_f32_16x16x32_bf16 v[14:17], v[196:199], v[162:165], v[14:17]
	v_mfma_f32_16x16x32_bf16 v[10:13], v[206:209], v[162:165], v[10:13]
	v_mfma_f32_16x16x32_bf16 v[6:9], v[196:199], v[170:173], v[6:9]
	v_mfma_f32_16x16x32_bf16 v[2:5], v[206:209], v[170:173], v[2:5]
	v_mfma_f32_16x16x32_bf16 v[46:49], v[200:203], v[150:153], v[46:49]
	v_mfma_f32_16x16x32_bf16 v[38:41], v[210:213], v[150:153], v[38:41]
	v_mfma_f32_16x16x32_bf16 v[30:33], v[200:203], v[158:161], v[30:33]
	v_mfma_f32_16x16x32_bf16 v[22:25], v[210:213], v[158:161], v[22:25]
	v_mfma_f32_16x16x32_bf16 v[14:17], v[200:203], v[166:169], v[14:17]
	v_mfma_f32_16x16x32_bf16 v[10:13], v[210:213], v[166:169], v[10:13]
	v_mfma_f32_16x16x32_bf16 v[6:9], v[200:203], v[174:177], v[6:9]
	v_mfma_f32_16x16x32_bf16 v[2:5], v[210:213], v[174:177], v[2:5]
	s_cmp_ge_i32 s60, s57
	s_barrier
	s_cbranch_scc1 .LBB0_1007
	s_mov_b64 s[26:27], s[28:29]
	s_branch .LBB0_1002

; #define PG8_STAGE(bufoff, gbase, voff) do { _Pragma("unroll") for (int _i = 0; _i < 2; ++_i) \
;         __builtin_amdgcn_global_load_lds((const unsigned*)((const char*)(gbase) + (voff)[_i]), (LAS unsigned*)(lds + (bufoff) + ldsw + _i * 8192), 16, 0, 0); } while (0)
; #define PG8_LDA(dst, b, h) do { _Pragma("unroll") for (int m = 0; m < 4; ++m) _Pragma("unroll") for (int k = 0; k < 2; ++k) dst[m][k] = *(const LAS bf16x8*)(lds + PG8_SA(b, h) + aoff + m * 2048 + k * 1024); } while (0)
; #define PG8_LDB(dst, b, h) do { _Pragma("unroll") for (int n = 0; n < 2; ++n) _Pragma("unroll") for (int k = 0; k < 2; ++k) dst[n][k] = *(const LAS bf16x8*)(lds + PG8_SB(b, h) + boff + n * 2048 + k * 1024); } while (0)
; #define PG8_MMA(ai, bj, At, Bt) do { __builtin_amdgcn_s_setprio(1); _Pragma("unroll") for (int m = 0; m < 4; ++m) _Pragma("unroll") for (int n = 0; n < 2; ++n) _Pragma("unroll") for (int k = 0; k < 2; ++k) \
;         acc[ai][bj][m][n] = __builtin_amdgcn_mfma_f32_16x16x32_bf16(Bt[n][k], At[m][k], acc[ai][bj][m][n], 0, 0, 0); __builtin_amdgcn_s_setprio(0); } while (0)
; #define PG8_WAIT_L(n) asm volatile("s_waitcnt lgkmcnt(" #n ")" ::: "memory")
; #define PG8_BAR __builtin_amdgcn_s_barrier()
; #define PG8_SCHED __builtin_amdgcn_sched_barrier(0)
; #define PG8_AOFF(u) do { const int _t = lt_tid(wvid); _Pragma("unroll") for (int _i = 0; _i < 2; ++_i) { int _R, _C; stage_rc(_t * 16 + _i * 8192, _R, _C); \
;         _Pragma("unroll") for (int _h = 0; _h < 2; ++_h) voffA[_h][_i] = (S.a_row(u, _h * HALF + _R) * (unsigned)K + (unsigned)(_C + (u).koff)) * 2u; } } while (0)
; template <class Epi, class Sched>
; __device__ __forceinline__ void gemm_phase(LAS unsigned char* lds, const bf16_t* Abase, const int K, const Sched& S, const Epi& E, const int wvid) {
;     ...
;             PG8_LDB(B0, 0, 0); PG8_SCHED; PG8_LDA(At, 0, 0); PG8_STAGE(PG8_SA(1, 1), a1, voffA[1]);
;             PG8_WAIT_L(8); PG8_BAR; PG8_WAIT_L(0); PG8_MMA(0, 0, At, B0); PG8_BAR; PG8_SCHED;
;             if (last && has_next) PG8_AOFF(nxt);
.LBB0_1209:
	v_add_u32_e32 v130, 0, v224
	v_add_u32_e32 v142, 0x10000, v130
	ds_read_b128 v[130:133], v142
	ds_read_b128 v[134:137], v142 offset:1024
	ds_read_b128 v[138:141], v142 offset:2048
	ds_read_b128 v[142:145], v142 offset:3072
	s_cmp_eq_u32 s23, 12
	s_cselect_b64 s[4:5], -1, 0
	s_add_i32 m0, s25, 0xc000
	s_add_u32 s28, s20, s26
	s_addc_u32 s29, s21, s27
	ds_read_b128 v[170:173], v226
	ds_read_b128 v[174:177], v226 offset:1024
	ds_read_b128 v[162:165], v226 offset:2048
	ds_read_b128 v[166:169], v226 offset:3072
	ds_read_b128 v[154:157], v226 offset:4096
	ds_read_b128 v[158:161], v226 offset:5120
	ds_read_b128 v[146:149], v226 offset:6144
	ds_read_b128 v[150:153], v226 offset:7168
	global_load_lds_dwordx4 v186, s[28:29]
	s_add_i32 m0, s25, 0xe000
	s_nop 0
	global_load_lds_dwordx4 v188, s[28:29]
	s_waitcnt lgkmcnt(8)
	s_barrier
	s_waitcnt lgkmcnt(0)
	s_waitcnt lgkmcnt(0)
	v_mfma_f32_16x16x32_bf16 v[126:129], v[130:133], v[170:173], v[126:129]
	v_mfma_f32_16x16x32_bf16 v[122:125], v[138:141], v[170:173], v[122:125]
	v_mfma_f32_16x16x32_bf16 v[118:121], v[130:133], v[162:165], v[118:121]
	v_mfma_f32_16x16x32_bf16 v[114:117], v[138:141], v[162:165], v[114:117]
	v_mfma_f32_16x16x32_bf16 v[110:113], v[130:133], v[154:157], v[110:113]
	v_mfma_f32_16x16x32_bf16 v[106:109], v[138:141], v[154:157], v[106:109]
	v_mfma_f32_16x16x32_bf16 v[94:97], v[130:133], v[146:149], v[94:97]
	v_mfma_f32_16x16x32_bf16 v[90:93], v[138:141], v[146:149], v[90:93]
	v_mfma_f32_16x16x32_bf16 v[126:129], v[134:137], v[174:177], v[126:129]
	v_mfma_f32_16x16x32_bf16 v[122:125], v[142:145], v[174:177], v[122:125]
	v_mfma_f32_16x16x32_bf16 v[118:121], v[134:137], v[166:169], v[118:121]
	v_mfma_f32_16x16x32_bf16 v[114:117], v[142:145], v[166:169], v[114:117]
	v_mfma_f32_16x16x32_bf16 v[110:113], v[134:137], v[158:161], v[110:113]
	v_mfma_f32_16x16x32_bf16 v[106:109], v[142:145], v[158:161], v[106:109]
	v_mfma_f32_16x16x32_bf16 v[94:97], v[134:137], v[150:153], v[94:97]
	v_mfma_f32_16x16x32_bf16 v[90:93], v[142:145], v[150:153], v[90:93]
	s_barrier
	s_and_b64 s[28:29], s[0:1], s[4:5]
	s_andn2_b64 vcc, exec, s[28:29]
	s_cbranch_vccnz .LBB0_1211
	v_mbcnt_lo_u32_b32 v0, -1, 0
	v_mbcnt_hi_u32_b32 v0, -1, v0
	v_mov_b32_e32 v189, v1
	v_or_b32_e32 v0, s75, v0
	v_ashrrev_i32_e32 v184, 31, v0
	v_lshrrev_b32_e32 v184, 26, v184
	v_lshlrev_b32_e32 v186, 4, v0
	v_add_u32_e32 v184, v0, v184
	v_bfe_i32 v0, v0, 27, 1
	v_lshrrev_b32_e32 v0, 22, v0
	v_add_u32_e32 v0, v186, v0
	v_and_b32_e32 v0, 0xfffffc00, v0
	v_sub_u32_e32 v0, v186, v0
	v_lshrrev_b32_e32 v185, 4, v0
	v_bitop3_b32 v0, v185, v0, 32 bitop3:0x6c
	v_ashrrev_i32_e32 v187, 31, v0
	v_ashrrev_i32_e32 v184, 6, v184
	v_lshrrev_b32_e32 v187, 26, v187
	v_lshlrev_b32_e32 v185, 3, v184
	v_add_u32_e32 v187, v0, v187
	v_and_b32_e32 v185, -16, v185
	v_ashrrev_i32_e32 v188, 6, v187
	v_add_u32_e32 v188, v188, v185
	v_and_b32_e32 v185, 0xc0, v187
	v_sub_u32_e32 v0, v0, v185
	v_lshlrev_b32_e32 v184, 5, v184
	v_ashrrev_i16_sdwa v0, v216, sext(v0) dst_sel:DWORD dst_unused:UNUSED_PAD src0_sel:DWORD src1_sel:BYTE_0
	v_and_b32_e32 v184, 32, v184
	v_bfe_i32 v0, v0, 0, 16
	v_add_lshl_u32 v0, v184, v0, 1
	v_add_u32_e32 v232, v188, v227
	v_min_i32_e32 v232, v232, v230
	v_add_u32_e32 v232, v232, v192
	v_ashrrev_i32_e32 v233, 31, v232
	v_lshl_add_u64 v[232:233], v[232:233], 2, s[10:11]
	global_load_dword v240, v[232:233], off
	v_add_u32_e32 v234, v188, v231
	v_min_i32_e32 v234, v234, v230
	v_add_u32_e32 v234, v234, v192
	v_ashrrev_i32_e32 v235, 31, v234
	v_lshl_add_u64 v[234:235], v[234:235], 2, s[10:11]
	global_load_dword v241, v[234:235], off
	v_add_u32_e32 v184, 0x2000, v186
	v_ashrrev_i32_e32 v185, 31, v184
	v_lshrrev_b32_e32 v185, 22, v185
	v_add_u32_e32 v185, v184, v185
	v_ashrrev_i32_e32 v185, 10, v185
	v_mul_i32_i24_e32 v186, 0x400, v185
	v_sub_u32_e32 v184, v184, v186
	v_lshrrev_b32_e32 v186, 4, v184
	v_bitop3_b32 v184, v186, v184, 32 bitop3:0x6c
	v_ashrrev_i32_e32 v187, 31, v184
	v_lshrrev_b32_e32 v187, 26, v187
	v_add_u32_e32 v187, v184, v187
	v_ashrrev_i32_e32 v188, 6, v187
	v_and_b32_e32 v187, 0xc0, v187
	v_lshlrev_b32_e32 v186, 3, v185
	v_sub_u32_e32 v184, v184, v187
	v_and_b32_e32 v186, -16, v186
	v_lshlrev_b32_e32 v185, 5, v185
	v_ashrrev_i16_sdwa v184, v216, sext(v184) dst_sel:DWORD dst_unused:UNUSED_PAD src0_sel:DWORD src1_sel:BYTE_0
	v_add_u32_e32 v186, v188, v186
	v_and_b32_e32 v185, 32, v185
	v_bfe_i32 v184, v184, 0, 16
	v_add_lshl_u32 v188, v185, v184, 1
	v_add_u32_e32 v236, v186, v227
	v_min_i32_e32 v236, v236, v230
	v_add_u32_e32 v236, v236, v192
	v_ashrrev_i32_e32 v237, 31, v236
	v_lshl_add_u64 v[236:237], v[236:237], 2, s[10:11]
	global_load_dword v242, v[236:237], off
	v_add_u32_e32 v238, v186, v231
	v_min_i32_e32 v238, v238, v230
	v_add_u32_e32 v238, v238, v192
	v_ashrrev_i32_e32 v239, 31, v238
	v_lshl_add_u64 v[238:239], v[238:239], 2, s[10:11]
	global_load_dword v243, v[238:239], off
	s_waitcnt vmcnt(0)
	v_lshl_add_u32 v200, v240, 11, v0
	v_lshl_add_u32 v0, v241, 11, v0
	v_mov_b64_e32 v[198:199], v[0:1]
	v_mov_b32_e32 v186, v0
	v_mov_b32_e32 v0, v200
	v_lshl_add_u32 v184, v242, 11, v188
	v_lshl_add_u32 v188, v243, 11, v188
	s_branch .LBB0_1212

; #define PG8_STAGE(bufoff, gbase, voff) do { _Pragma("unroll") for (int _i = 0; _i < 2; ++_i) \
;         __builtin_amdgcn_global_load_lds((const unsigned*)((const char*)(gbase) + (voff)[_i]), (LAS unsigned*)(lds + (bufoff) + ldsw + _i * 8192), 16, 0, 0); } while (0)
; #define PG8_LDA(dst, b, h) do { _Pragma("unroll") for (int m = 0; m < 4; ++m) _Pragma("unroll") for (int k = 0; k < 2; ++k) dst[m][k] = *(const LAS bf16x8*)(lds + PG8_SA(b, h) + aoff + m * 2048 + k * 1024); } while (0)
; #define PG8_LDB(dst, b, h) do { _Pragma("unroll") for (int n = 0; n < 2; ++n) _Pragma("unroll") for (int k = 0; k < 2; ++k) dst[n][k] = *(const LAS bf16x8*)(lds + PG8_SB(b, h) + boff + n * 2048 + k * 1024); } while (0)
; #define PG8_MMA(ai, bj, At, Bt) do { __builtin_amdgcn_s_setprio(1); _Pragma("unroll") for (int m = 0; m < 4; ++m) _Pragma("unroll") for (int n = 0; n < 2; ++n) _Pragma("unroll") for (int k = 0; k < 2; ++k) \
;         acc[ai][bj][m][n] = __builtin_amdgcn_mfma_f32_16x16x32_bf16(Bt[n][k], At[m][k], acc[ai][bj][m][n], 0, 0, 0); __builtin_amdgcn_s_setprio(0); } while (0)
; #define PG8_WAIT_V(n) asm volatile("s_waitcnt vmcnt(" #n ")" ::: "memory")
; #define PG8_WAIT_L(n) asm volatile("s_waitcnt lgkmcnt(" #n ")" ::: "memory")
; #define PG8_BAR __builtin_amdgcn_s_barrier()
; #define PG8_SCHED __builtin_amdgcn_sched_barrier(0)
; template <class Epi, class Sched>
; __device__ __forceinline__ void gemm_phase(LAS unsigned char* lds, const bf16_t* Abase, const int K, const Sched& S, const Epi& E, const int wvid) {
;     ...
;             const char* a2 = last ? Ab : Ab + (size_t)(t + 2) * kstep; const char* b2 = last ? nB : cB + (size_t)(t + 2) * kstep;
;             const char* a3 = a2 + kstep; const char* b3 = b2 + kstep;
;             PG8_LDB(B1, 0, 1); PG8_STAGE(PG8_SB(0, 0), b2, voffB);
;             PG8_BAR; PG8_WAIT_L(0); PG8_MMA(0, 1, At, B1); PG8_BAR;
;             PG8_LDA(At, 0, 1); PG8_STAGE(PG8_SA(0, 0), a2, voffA[0]);
;             PG8_BAR; PG8_WAIT_L(0); PG8_MMA(1, 0, At, B0); PG8_BAR; PG8_SCHED;
;             PG8_STAGE(PG8_SB(0, 1), b2 + hstep, voffB);
;             PG8_WAIT_V(6); PG8_BAR; PG8_MMA(1, 1, At, B1); PG8_BAR;
;             PG8_LDB(B0, 1, 0); PG8_SCHED; PG8_LDA(At, 1, 0); PG8_STAGE(PG8_SA(0, 1), a2, voffA[1]);
.LBB0_1212:
	s_add_u32 s28, s26, 0x100
	s_addc_u32 s29, s27, 0
	s_and_b64 s[30:31], s[4:5], exec
	s_cselect_b32 s30, 0, s28
	s_cselect_b32 s31, 0, s29
	s_add_u32 s30, s16, s30
	v_lshl_add_u64 v[236:237], v[196:197], 0, s[26:27]
	s_addc_u32 s31, s17, s31
	s_add_i32 s26, 0, 0x14000
	v_cndmask_b32_e64 v237, v237, v191, s[4:5]
	v_cndmask_b32_e64 v236, v236, v229, s[4:5]
	s_mov_b32 m0, s39
	v_add_u32_e32 v185, s26, v224
	v_lshl_add_u64 v[238:239], v[236:237], 0, v[180:181]
	ds_read_b128 v[200:203], v185
	ds_read_b128 v[206:209], v185 offset:1024
	ds_read_b128 v[210:213], v185 offset:2048
	ds_read_b128 v[232:235], v185 offset:3072
	global_load_lds_dwordx4 v[238:239], off
	v_lshl_add_u64 v[240:241], v[236:237], 0, v[182:183]
	s_mov_b32 m0, s42
	s_nop 0
	global_load_lds_dwordx4 v[240:241], off
	s_barrier
	s_waitcnt lgkmcnt(0)
	s_waitcnt lgkmcnt(0)
	v_mfma_f32_16x16x32_bf16 v[102:105], v[200:203], v[170:173], v[102:105]
	v_mfma_f32_16x16x32_bf16 v[98:101], v[210:213], v[170:173], v[98:101]
	v_mfma_f32_16x16x32_bf16 v[86:89], v[200:203], v[162:165], v[86:89]
	v_mfma_f32_16x16x32_bf16 v[82:85], v[210:213], v[162:165], v[82:85]
	v_mfma_f32_16x16x32_bf16 v[78:81], v[200:203], v[154:157], v[78:81]
	v_mfma_f32_16x16x32_bf16 v[74:77], v[210:213], v[154:157], v[74:77]
	v_mfma_f32_16x16x32_bf16 v[70:73], v[200:203], v[146:149], v[70:73]
	v_mfma_f32_16x16x32_bf16 v[66:69], v[210:213], v[146:149], v[66:69]
	v_mfma_f32_16x16x32_bf16 v[102:105], v[206:209], v[174:177], v[102:105]
	v_mfma_f32_16x16x32_bf16 v[98:101], v[232:235], v[174:177], v[98:101]
	v_mfma_f32_16x16x32_bf16 v[86:89], v[206:209], v[166:169], v[86:89]
	v_mfma_f32_16x16x32_bf16 v[82:85], v[232:235], v[166:169], v[82:85]
	v_mfma_f32_16x16x32_bf16 v[78:81], v[206:209], v[158:161], v[78:81]
	v_mfma_f32_16x16x32_bf16 v[74:77], v[232:235], v[158:161], v[74:77]
	v_mfma_f32_16x16x32_bf16 v[70:73], v[206:209], v[150:153], v[70:73]
	v_mfma_f32_16x16x32_bf16 v[66:69], v[232:235], v[150:153], v[66:69]
	s_mov_b32 m0, s25
	s_barrier
	ds_read_b128 v[146:149], v226 offset:16384
	ds_read_b128 v[150:153], v226 offset:17408
	ds_read_b128 v[154:157], v226 offset:18432
	ds_read_b128 v[158:161], v226 offset:19456
	ds_read_b128 v[162:165], v226 offset:20480
	ds_read_b128 v[166:169], v226 offset:21504
	ds_read_b128 v[170:173], v226 offset:22528
	ds_read_b128 v[174:177], v226 offset:23552
	global_load_lds_dwordx4 v0, s[30:31]
	s_mov_b32 m0, s43
	v_mov_b32_e32 v185, v1
	global_load_lds_dwordx4 v184, s[30:31]
	s_barrier
	s_waitcnt lgkmcnt(0)
	v_lshl_add_u64 v[242:243], s[30:31], 0, v[0:1]
	v_lshl_add_u64 v[244:245], s[30:31], 0, v[184:185]
	s_waitcnt lgkmcnt(0)
	v_mfma_f32_16x16x32_bf16 v[62:65], v[130:133], v[146:149], v[62:65]
	v_mfma_f32_16x16x32_bf16 v[58:61], v[138:141], v[146:149], v[58:61]
	v_mfma_f32_16x16x32_bf16 v[46:49], v[130:133], v[154:157], v[46:49]
	v_mfma_f32_16x16x32_bf16 v[42:45], v[138:141], v[154:157], v[42:45]
	v_mfma_f32_16x16x32_bf16 v[30:33], v[130:133], v[162:165], v[30:33]
	v_mfma_f32_16x16x32_bf16 v[26:29], v[138:141], v[162:165], v[26:29]
	v_mfma_f32_16x16x32_bf16 v[14:17], v[130:133], v[170:173], v[14:17]
	v_mfma_f32_16x16x32_bf16 v[10:13], v[138:141], v[170:173], v[10:13]
	v_mfma_f32_16x16x32_bf16 v[62:65], v[134:137], v[150:153], v[62:65]
	v_mfma_f32_16x16x32_bf16 v[58:61], v[142:145], v[150:153], v[58:61]
	v_mfma_f32_16x16x32_bf16 v[46:49], v[134:137], v[158:161], v[46:49]
	v_mfma_f32_16x16x32_bf16 v[42:45], v[142:145], v[158:161], v[42:45]
	v_mfma_f32_16x16x32_bf16 v[30:33], v[134:137], v[166:169], v[30:33]
	v_mfma_f32_16x16x32_bf16 v[26:29], v[142:145], v[166:169], v[26:29]
	v_mfma_f32_16x16x32_bf16 v[14:17], v[134:137], v[174:177], v[14:17]
	v_mfma_f32_16x16x32_bf16 v[10:13], v[142:145], v[174:177], v[10:13]
	s_barrier
	v_lshl_add_u64 v[130:131], v[236:237], 0, s[90:91]
	s_add_i32 s4, s26, s38
	v_lshl_add_u64 v[132:133], v[130:131], 0, v[180:181]
	s_mov_b32 m0, s4
	v_lshl_add_u64 v[130:131], v[130:131], 0, v[182:183]
	global_load_lds_dwordx4 v[132:133], off
	s_add_i32 m0, s4, 0x2000
	s_nop 0
	global_load_lds_dwordx4 v[130:131], off
	s_waitcnt vmcnt(6)
	s_barrier
	v_mfma_f32_16x16x32_bf16 v[54:57], v[200:203], v[146:149], v[54:57]
	v_mfma_f32_16x16x32_bf16 v[50:53], v[210:213], v[146:149], v[50:53]
	v_mfma_f32_16x16x32_bf16 v[38:41], v[200:203], v[154:157], v[38:41]
	v_mfma_f32_16x16x32_bf16 v[34:37], v[210:213], v[154:157], v[34:37]
	v_mfma_f32_16x16x32_bf16 v[22:25], v[200:203], v[162:165], v[22:25]
	v_mfma_f32_16x16x32_bf16 v[18:21], v[210:213], v[162:165], v[18:21]
	v_mfma_f32_16x16x32_bf16 v[6:9], v[200:203], v[170:173], v[6:9]
	v_mfma_f32_16x16x32_bf16 v[2:5], v[210:213], v[170:173], v[2:5]
	v_mfma_f32_16x16x32_bf16 v[54:57], v[206:209], v[150:153], v[54:57]
	v_mfma_f32_16x16x32_bf16 v[50:53], v[232:235], v[150:153], v[50:53]
	v_mfma_f32_16x16x32_bf16 v[38:41], v[206:209], v[158:161], v[38:41]
	v_mfma_f32_16x16x32_bf16 v[34:37], v[232:235], v[158:161], v[34:37]
	v_mfma_f32_16x16x32_bf16 v[22:25], v[206:209], v[166:169], v[22:25]
	v_mfma_f32_16x16x32_bf16 v[18:21], v[232:235], v[166:169], v[18:21]
	v_mfma_f32_16x16x32_bf16 v[6:9], v[206:209], v[174:177], v[6:9]
	v_mfma_f32_16x16x32_bf16 v[2:5], v[232:235], v[174:177], v[2:5]
	s_add_i32 s4, 0, 0x18000
	v_add_u32_e32 v142, s4, v224
	s_barrier
	ds_read_b128 v[130:133], v142
	ds_read_b128 v[134:137], v142 offset:1024
	ds_read_b128 v[138:141], v142 offset:2048
	ds_read_b128 v[142:145], v142 offset:3072
	s_mov_b32 m0, s46
	v_lshl_add_u64 v[198:199], s[30:31], 0, v[198:199]
	ds_read_b128 v[146:149], v226 offset:32768
	ds_read_b128 v[150:153], v226 offset:33792
	ds_read_b128 v[154:157], v226 offset:34816
	ds_read_b128 v[158:161], v226 offset:35840
	ds_read_b128 v[162:165], v226 offset:36864
	ds_read_b128 v[166:169], v226 offset:37888
	ds_read_b128 v[170:173], v226 offset:38912
	ds_read_b128 v[174:177], v226 offset:39936
	global_load_lds_dwordx4 v[198:199], off
	v_lshl_add_u64 v[198:199], s[30:31], 0, v[188:189]
	s_mov_b32 m0, s47
	s_nop 0
	global_load_lds_dwordx4 v[198:199], off
	s_waitcnt lgkmcnt(8)
	s_barrier
; #define PG8_STAGE(bufoff, gbase, voff) do { _Pragma("unroll") for (int _i = 0; _i < 2; ++_i) \
;         __builtin_amdgcn_global_load_lds((const unsigned*)((const char*)(gbase) + (voff)[_i]), (LAS unsigned*)(lds + (bufoff) + ldsw + _i * 8192), 16, 0, 0); } while (0)
; #define PG8_LDA(dst, b, h) do { _Pragma("unroll") for (int m = 0; m < 4; ++m) _Pragma("unroll") for (int k = 0; k < 2; ++k) dst[m][k] = *(const LAS bf16x8*)(lds + PG8_SA(b, h) + aoff + m * 2048 + k * 1024); } while (0)
; #define PG8_LDB(dst, b, h) do { _Pragma("unroll") for (int n = 0; n < 2; ++n) _Pragma("unroll") for (int k = 0; k < 2; ++k) dst[n][k] = *(const LAS bf16x8*)(lds + PG8_SB(b, h) + boff + n * 2048 + k * 1024); } while (0)
; #define PG8_MMA(ai, bj, At, Bt) do { __builtin_amdgcn_s_setprio(1); _Pragma("unroll") for (int m = 0; m < 4; ++m) _Pragma("unroll") for (int n = 0; n < 2; ++n) _Pragma("unroll") for (int k = 0; k < 2; ++k) \
;         acc[ai][bj][m][n] = __builtin_amdgcn_mfma_f32_16x16x32_bf16(Bt[n][k], At[m][k], acc[ai][bj][m][n], 0, 0, 0); __builtin_amdgcn_s_setprio(0); } while (0)
; #define PG8_WAIT_V(n) asm volatile("s_waitcnt vmcnt(" #n ")" ::: "memory")
; #define PG8_WAIT_L(n) asm volatile("s_waitcnt lgkmcnt(" #n ")" ::: "memory")
; #define PG8_BAR __builtin_amdgcn_s_barrier()
; #define PG8_SCHED __builtin_amdgcn_sched_barrier(0)
; template <class Epi, class Sched>
; __device__ __forceinline__ void gemm_phase(LAS unsigned char* lds, const bf16_t* Abase, const int K, const Sched& S, const Epi& E, const int wvid) {
;     ...
;             PG8_WAIT_L(8); PG8_BAR; PG8_WAIT_L(0); PG8_MMA(0, 0, At, B0); PG8_BAR; PG8_SCHED;
;             PG8_LDB(B1, 1, 1); PG8_STAGE(PG8_SB(1, 0), b3, voffB);
;             PG8_BAR; PG8_WAIT_L(0); PG8_MMA(0, 1, At, B1); PG8_BAR;
;             PG8_LDA(At, 1, 1); PG8_STAGE(PG8_SA(1, 0), a3, voffA[0]);
;             PG8_BAR; PG8_WAIT_L(0); PG8_MMA(1, 0, At, B0); PG8_BAR; PG8_SCHED;
;             PG8_STAGE(PG8_SB(1, 1), b3 + hstep, voffB);
;             PG8_WAIT_V(6); PG8_BAR; PG8_MMA(1, 1, At, B1); PG8_BAR;
;         }
	s_waitcnt lgkmcnt(0)
	s_waitcnt lgkmcnt(0)
	v_mfma_f32_16x16x32_bf16 v[126:129], v[130:133], v[146:149], v[126:129]
	v_mfma_f32_16x16x32_bf16 v[122:125], v[138:141], v[146:149], v[122:125]
	v_mfma_f32_16x16x32_bf16 v[118:121], v[130:133], v[154:157], v[118:121]
	v_mfma_f32_16x16x32_bf16 v[114:117], v[138:141], v[154:157], v[114:117]
	v_mfma_f32_16x16x32_bf16 v[110:113], v[130:133], v[162:165], v[110:113]
	v_mfma_f32_16x16x32_bf16 v[106:109], v[138:141], v[162:165], v[106:109]
	v_mfma_f32_16x16x32_bf16 v[94:97], v[130:133], v[170:173], v[94:97]
	v_mfma_f32_16x16x32_bf16 v[90:93], v[138:141], v[170:173], v[90:93]
	v_mfma_f32_16x16x32_bf16 v[126:129], v[134:137], v[150:153], v[126:129]
	v_mfma_f32_16x16x32_bf16 v[122:125], v[142:145], v[150:153], v[122:125]
	v_mfma_f32_16x16x32_bf16 v[118:121], v[134:137], v[158:161], v[118:121]
	v_mfma_f32_16x16x32_bf16 v[114:117], v[142:145], v[158:161], v[114:117]
	v_mfma_f32_16x16x32_bf16 v[110:113], v[134:137], v[166:169], v[110:113]
	v_mfma_f32_16x16x32_bf16 v[106:109], v[142:145], v[166:169], v[106:109]
	v_mfma_f32_16x16x32_bf16 v[94:97], v[134:137], v[174:177], v[94:97]
	v_mfma_f32_16x16x32_bf16 v[90:93], v[142:145], v[174:177], v[90:93]
	s_barrier
	s_add_i32 s5, 0, 0x1c000
	s_add_i32 s4, s4, s38
	v_add_u32_e32 v185, s5, v224
	v_lshl_add_u64 v[202:203], v[238:239], 0, s[12:13]
	s_mov_b32 m0, s4
	ds_read_b128 v[198:201], v185
	ds_read_b128 v[206:209], v185 offset:1024
	ds_read_b128 v[210:213], v185 offset:2048
	ds_read_b128 v[232:235], v185 offset:3072
	global_load_lds_dwordx4 v[202:203], off
	v_lshl_add_u64 v[202:203], v[240:241], 0, s[12:13]
	s_add_i32 m0, s4, 0x2000
	s_nop 0
	global_load_lds_dwordx4 v[202:203], off
	s_barrier
	s_waitcnt lgkmcnt(0)
	s_waitcnt lgkmcnt(0)
	v_mfma_f32_16x16x32_bf16 v[102:105], v[198:201], v[146:149], v[102:105]
	v_mfma_f32_16x16x32_bf16 v[98:101], v[210:213], v[146:149], v[98:101]
	v_mfma_f32_16x16x32_bf16 v[86:89], v[198:201], v[154:157], v[86:89]
	v_mfma_f32_16x16x32_bf16 v[82:85], v[210:213], v[154:157], v[82:85]
	v_mfma_f32_16x16x32_bf16 v[78:81], v[198:201], v[162:165], v[78:81]
	v_mfma_f32_16x16x32_bf16 v[74:77], v[210:213], v[162:165], v[74:77]
	v_mfma_f32_16x16x32_bf16 v[70:73], v[198:201], v[170:173], v[70:73]
	v_mfma_f32_16x16x32_bf16 v[66:69], v[210:213], v[170:173], v[66:69]
	v_mfma_f32_16x16x32_bf16 v[102:105], v[206:209], v[150:153], v[102:105]
	v_mfma_f32_16x16x32_bf16 v[98:101], v[232:235], v[150:153], v[98:101]
	v_mfma_f32_16x16x32_bf16 v[86:89], v[206:209], v[158:161], v[86:89]
	v_mfma_f32_16x16x32_bf16 v[82:85], v[232:235], v[158:161], v[82:85]
	v_mfma_f32_16x16x32_bf16 v[78:81], v[206:209], v[166:169], v[78:81]
	v_mfma_f32_16x16x32_bf16 v[74:77], v[232:235], v[166:169], v[74:77]
	v_mfma_f32_16x16x32_bf16 v[70:73], v[206:209], v[174:177], v[70:73]
	v_mfma_f32_16x16x32_bf16 v[66:69], v[232:235], v[174:177], v[66:69]
	s_mov_b32 m0, s48
	v_lshl_add_u64 v[202:203], v[242:243], 0, s[12:13]
	s_barrier
	ds_read_b128 v[146:149], v226 offset:49152
	ds_read_b128 v[150:153], v226 offset:50176
	ds_read_b128 v[154:157], v226 offset:51200
	ds_read_b128 v[158:161], v226 offset:52224
	ds_read_b128 v[162:165], v226 offset:53248
	ds_read_b128 v[166:169], v226 offset:54272
	ds_read_b128 v[170:173], v226 offset:55296
	ds_read_b128 v[174:177], v226 offset:56320
	global_load_lds_dwordx4 v[202:203], off
	v_lshl_add_u64 v[202:203], v[244:245], 0, s[12:13]
	s_mov_b32 m0, s49
	s_nop 0
	global_load_lds_dwordx4 v[202:203], off
	s_barrier
	s_waitcnt lgkmcnt(0)
	s_waitcnt lgkmcnt(0)
	v_mfma_f32_16x16x32_bf16 v[62:65], v[130:133], v[146:149], v[62:65]
	v_mfma_f32_16x16x32_bf16 v[58:61], v[138:141], v[146:149], v[58:61]
	v_mfma_f32_16x16x32_bf16 v[46:49], v[130:133], v[154:157], v[46:49]
	v_mfma_f32_16x16x32_bf16 v[42:45], v[138:141], v[154:157], v[42:45]
	v_mfma_f32_16x16x32_bf16 v[30:33], v[130:133], v[162:165], v[30:33]
	v_mfma_f32_16x16x32_bf16 v[26:29], v[138:141], v[162:165], v[26:29]
	v_mfma_f32_16x16x32_bf16 v[14:17], v[130:133], v[170:173], v[14:17]
	v_mfma_f32_16x16x32_bf16 v[10:13], v[138:141], v[170:173], v[10:13]
	v_mfma_f32_16x16x32_bf16 v[62:65], v[134:137], v[150:153], v[62:65]
	v_mfma_f32_16x16x32_bf16 v[58:61], v[142:145], v[150:153], v[58:61]
	v_mfma_f32_16x16x32_bf16 v[46:49], v[134:137], v[158:161], v[46:49]
	v_mfma_f32_16x16x32_bf16 v[42:45], v[142:145], v[158:161], v[42:45]
	v_mfma_f32_16x16x32_bf16 v[30:33], v[134:137], v[166:169], v[30:33]
	v_mfma_f32_16x16x32_bf16 v[26:29], v[142:145], v[166:169], v[26:29]
	v_mfma_f32_16x16x32_bf16 v[14:17], v[134:137], v[174:177], v[14:17]
	v_mfma_f32_16x16x32_bf16 v[10:13], v[142:145], v[174:177], v[10:13]
	s_barrier
	v_lshl_add_u64 v[130:131], v[236:237], 0, s[14:15]
	s_add_i32 s4, s5, s38
	v_lshl_add_u64 v[132:133], v[130:131], 0, v[180:181]
	s_mov_b32 m0, s4
	v_lshl_add_u64 v[130:131], v[130:131], 0, v[182:183]
	global_load_lds_dwordx4 v[132:133], off
	s_add_i32 m0, s4, 0x2000
	s_nop 0
	global_load_lds_dwordx4 v[130:131], off
	s_waitcnt vmcnt(6)
	s_barrier
	v_mfma_f32_16x16x32_bf16 v[54:57], v[198:201], v[146:149], v[54:57]
	v_mfma_f32_16x16x32_bf16 v[50:53], v[210:213], v[146:149], v[50:53]
	v_mfma_f32_16x16x32_bf16 v[38:41], v[198:201], v[154:157], v[38:41]
	v_mfma_f32_16x16x32_bf16 v[34:37], v[210:213], v[154:157], v[34:37]
	v_mfma_f32_16x16x32_bf16 v[22:25], v[198:201], v[162:165], v[22:25]
	v_mfma_f32_16x16x32_bf16 v[18:21], v[210:213], v[162:165], v[18:21]
	v_mfma_f32_16x16x32_bf16 v[6:9], v[198:201], v[170:173], v[6:9]
	v_mfma_f32_16x16x32_bf16 v[2:5], v[210:213], v[170:173], v[2:5]
	v_mfma_f32_16x16x32_bf16 v[54:57], v[206:209], v[150:153], v[54:57]
	v_mfma_f32_16x16x32_bf16 v[50:53], v[232:235], v[150:153], v[50:53]
	v_mfma_f32_16x16x32_bf16 v[38:41], v[206:209], v[158:161], v[38:41]
	v_mfma_f32_16x16x32_bf16 v[34:37], v[232:235], v[158:161], v[34:37]
	v_mfma_f32_16x16x32_bf16 v[22:25], v[206:209], v[166:169], v[22:25]
	v_mfma_f32_16x16x32_bf16 v[18:21], v[232:235], v[166:169], v[18:21]
	v_mfma_f32_16x16x32_bf16 v[6:9], v[206:209], v[174:177], v[6:9]
	v_mfma_f32_16x16x32_bf16 v[2:5], v[232:235], v[174:177], v[2:5]
	s_add_i32 s23, s23, 2
	s_cmp_gt_u32 s23, 13
	s_barrier
	s_cbranch_scc1 .LBB0_1214
	s_mov_b64 s[26:27], s[28:29]
	s_branch .LBB0_1209

; #define PG8_STAGE(bufoff, gbase, voff) do { _Pragma("unroll") for (int _i = 0; _i < 2; ++_i) \
;         __builtin_amdgcn_global_load_lds((const unsigned*)((const char*)(gbase) + (voff)[_i]), (LAS unsigned*)(lds + (bufoff) + ldsw + _i * 8192), 16, 0, 0); } while (0)
; #define PG8_LDA(dst, b, h) do { _Pragma("unroll") for (int m = 0; m < 4; ++m) _Pragma("unroll") for (int k = 0; k < 2; ++k) dst[m][k] = *(const LAS bf16x8*)(lds + PG8_SA(b, h) + aoff + m * 2048 + k * 1024); } while (0)
; #define PG8_LDB(dst, b, h) do { _Pragma("unroll") for (int n = 0; n < 2; ++n) _Pragma("unroll") for (int k = 0; k < 2; ++k) dst[n][k] = *(const LAS bf16x8*)(lds + PG8_SB(b, h) + boff + n * 2048 + k * 1024); } while (0)
; #define PG8_MMA(ai, bj, At, Bt) do { __builtin_amdgcn_s_setprio(1); _Pragma("unroll") for (int m = 0; m < 4; ++m) _Pragma("unroll") for (int n = 0; n < 2; ++n) _Pragma("unroll") for (int k = 0; k < 2; ++k) \
;         acc[ai][bj][m][n] = __builtin_amdgcn_mfma_f32_16x16x32_bf16(Bt[n][k], At[m][k], acc[ai][bj][m][n], 0, 0, 0); __builtin_amdgcn_s_setprio(0); } while (0)
; #define PG8_WAIT_L(n) asm volatile("s_waitcnt lgkmcnt(" #n ")" ::: "memory")
; #define PG8_BAR __builtin_amdgcn_s_barrier()
; #define PG8_SCHED __builtin_amdgcn_sched_barrier(0)
; #define PG8_AOFF(u) do { const int _t = lt_tid(wvid); _Pragma("unroll") for (int _i = 0; _i < 2; ++_i) { int _R, _C; stage_rc(_t * 16 + _i * 8192, _R, _C); \
;         _Pragma("unroll") for (int _h = 0; _h < 2; ++_h) voffA[_h][_i] = (S.a_row(u, _h * HALF + _R) * (unsigned)K + (unsigned)(_C + (u).koff)) * 2u; } } while (0)
; template <class Epi, class Sched>
; __device__ __forceinline__ void gemm_phase(LAS unsigned char* lds, const bf16_t* Abase, const int K, const Sched& S, const Epi& E, const int wvid) {
;     ...
;             PG8_LDB(B0, 0, 0); PG8_SCHED; PG8_LDA(At, 0, 0); PG8_STAGE(PG8_SA(1, 1), a1, voffA[1]);
;             PG8_WAIT_L(8); PG8_BAR; PG8_WAIT_L(0); PG8_MMA(0, 0, At, B0); PG8_BAR; PG8_SCHED;
;             if (last && has_next) PG8_AOFF(nxt);
.LBB0_1476:
	s_waitcnt vmcnt(0)
	v_add_u32_e32 v130, 0, v223
	v_add_u32_e32 v142, 0x10000, v130
	ds_read_b128 v[130:133], v142
	ds_read_b128 v[134:137], v142 offset:1024
	ds_read_b128 v[138:141], v142 offset:2048
	ds_read_b128 v[142:145], v142 offset:3072
	s_cmp_eq_u32 s25, 4
	s_cselect_b64 s[4:5], -1, 0
	s_add_i32 m0, s17, 0xc000
	s_add_u32 s28, s22, s26
	s_addc_u32 s29, s23, s27
	ds_read_b128 v[170:173], v225
	ds_read_b128 v[174:177], v225 offset:1024
	ds_read_b128 v[162:165], v225 offset:2048
	ds_read_b128 v[166:169], v225 offset:3072
	ds_read_b128 v[154:157], v225 offset:4096
	ds_read_b128 v[158:161], v225 offset:5120
	ds_read_b128 v[146:149], v225 offset:6144
	ds_read_b128 v[150:153], v225 offset:7168
	global_load_lds_dwordx4 v184, s[28:29]
	s_add_i32 m0, s17, 0xe000
	s_nop 0
	global_load_lds_dwordx4 v188, s[28:29]
	s_waitcnt lgkmcnt(8)
	s_barrier
	s_waitcnt lgkmcnt(0)
	s_waitcnt lgkmcnt(0)
	v_mfma_f32_16x16x32_bf16 v[126:129], v[130:133], v[170:173], v[126:129]
	v_mfma_f32_16x16x32_bf16 v[122:125], v[138:141], v[170:173], v[122:125]
	v_mfma_f32_16x16x32_bf16 v[118:121], v[130:133], v[162:165], v[118:121]
	v_mfma_f32_16x16x32_bf16 v[114:117], v[138:141], v[162:165], v[114:117]
	v_mfma_f32_16x16x32_bf16 v[110:113], v[130:133], v[154:157], v[110:113]
	v_mfma_f32_16x16x32_bf16 v[106:109], v[138:141], v[154:157], v[106:109]
	v_mfma_f32_16x16x32_bf16 v[102:105], v[130:133], v[146:149], v[102:105]
	v_mfma_f32_16x16x32_bf16 v[98:101], v[138:141], v[146:149], v[98:101]
	v_mfma_f32_16x16x32_bf16 v[126:129], v[134:137], v[174:177], v[126:129]
	v_mfma_f32_16x16x32_bf16 v[122:125], v[142:145], v[174:177], v[122:125]
	v_mfma_f32_16x16x32_bf16 v[118:121], v[134:137], v[166:169], v[118:121]
	v_mfma_f32_16x16x32_bf16 v[114:117], v[142:145], v[166:169], v[114:117]
	v_mfma_f32_16x16x32_bf16 v[110:113], v[134:137], v[158:161], v[110:113]
	v_mfma_f32_16x16x32_bf16 v[106:109], v[142:145], v[158:161], v[106:109]
	v_mfma_f32_16x16x32_bf16 v[102:105], v[134:137], v[150:153], v[102:105]
	v_mfma_f32_16x16x32_bf16 v[98:101], v[142:145], v[150:153], v[98:101]
	s_barrier
	s_and_b64 s[28:29], s[0:1], s[4:5]
	s_andn2_b64 vcc, exec, s[28:29]
	s_cbranch_vccnz .LBB0_1478
	v_mbcnt_lo_u32_b32 v0, -1, 0
	v_mbcnt_hi_u32_b32 v0, -1, v0
	s_nop 0
	v_or_b32_e32 v0, s75, v0
	v_ashrrev_i32_e32 v185, 31, v0
	v_lshrrev_b32_e32 v185, 26, v185
	v_lshlrev_b32_e32 v184, 4, v0
	v_add_u32_e32 v185, v0, v185
	v_bfe_i32 v0, v0, 27, 1
	v_lshrrev_b32_e32 v0, 22, v0
	v_add_u32_e32 v0, v184, v0
	v_and_b32_e32 v0, 0xfffffc00, v0
	v_sub_u32_e32 v0, v184, v0
	v_lshrrev_b32_e32 v186, 4, v0
	v_bitop3_b32 v0, v186, v0, 32 bitop3:0x6c
	v_ashrrev_i32_e32 v187, 31, v0
	v_lshrrev_b32_e32 v187, 26, v187
	v_add_u32_e32 v187, v0, v187
	v_ashrrev_i32_e32 v185, 6, v185
	v_ashrrev_i32_e32 v188, 6, v187
	v_and_b32_e32 v187, 0xc0, v187
	v_lshlrev_b32_e32 v186, 3, v185
	v_sub_u32_e32 v0, v0, v187
	v_and_b32_e32 v186, -16, v186
	v_lshlrev_b32_e32 v185, 5, v185
	v_ashrrev_i16_sdwa v0, v216, sext(v0) dst_sel:DWORD dst_unused:UNUSED_PAD src0_sel:DWORD src1_sel:BYTE_0
	v_add_u32_e32 v186, v188, v186
	v_and_b32_e32 v185, 32, v185
	v_bfe_i32 v0, v0, 0, 16
	v_add_lshl_u32 v0, v185, v0, 1
	v_add_u32_e32 v185, v186, v228
	v_add_u32_e32 v186, v186, v230
	v_add_u32_e32 v184, 0x2000, v184
	v_lshl_add_u32 v185, v185, 10, v0
	v_lshl_add_u32 v0, v186, 10, v0
	v_ashrrev_i32_e32 v186, 31, v184
	v_lshrrev_b32_e32 v186, 22, v186
	v_add_u32_e32 v186, v184, v186
	v_ashrrev_i32_e32 v186, 10, v186
	v_mul_i32_i24_e32 v187, 0x400, v186
	v_sub_u32_e32 v184, v184, v187
	v_lshrrev_b32_e32 v187, 4, v184
	v_bitop3_b32 v184, v187, v184, 32 bitop3:0x6c
	v_ashrrev_i32_e32 v188, 31, v184
	v_lshrrev_b32_e32 v188, 26, v188
	v_add_u32_e32 v188, v184, v188
	v_ashrrev_i32_e32 v189, 6, v188
	v_and_b32_e32 v188, 0xc0, v188
	v_lshlrev_b32_e32 v187, 3, v186
	v_sub_u32_e32 v184, v184, v188
	v_and_b32_e32 v187, -16, v187
	v_lshlrev_b32_e32 v186, 5, v186
	v_ashrrev_i16_sdwa v184, v216, sext(v184) dst_sel:DWORD dst_unused:UNUSED_PAD src0_sel:DWORD src1_sel:BYTE_0
	v_add_u32_e32 v187, v189, v187
	v_and_b32_e32 v186, 32, v186
	v_bfe_i32 v184, v184, 0, 16
	v_add_lshl_u32 v184, v186, v184, 1
	v_add_u32_e32 v186, v187, v228
	v_add_u32_e32 v187, v187, v230
	v_lshl_add_u32 v186, v186, 10, v184
	v_lshl_add_u32 v188, v187, 10, v184
	v_mov_b32_e32 v189, v1
	v_mov_b64_e32 v[198:199], v[0:1]
	v_mov_b32_e32 v184, v0
	v_mov_b32_e32 v0, v185
	s_branch .LBB0_1479

; #define PG8_STAGE(bufoff, gbase, voff) do { _Pragma("unroll") for (int _i = 0; _i < 2; ++_i) \
;         __builtin_amdgcn_global_load_lds((const unsigned*)((const char*)(gbase) + (voff)[_i]), (LAS unsigned*)(lds + (bufoff) + ldsw + _i * 8192), 16, 0, 0); } while (0)
; #define PG8_LDA(dst, b, h) do { _Pragma("unroll") for (int m = 0; m < 4; ++m) _Pragma("unroll") for (int k = 0; k < 2; ++k) dst[m][k] = *(const LAS bf16x8*)(lds + PG8_SA(b, h) + aoff + m * 2048 + k * 1024); } while (0)
; #define PG8_LDB(dst, b, h) do { _Pragma("unroll") for (int n = 0; n < 2; ++n) _Pragma("unroll") for (int k = 0; k < 2; ++k) dst[n][k] = *(const LAS bf16x8*)(lds + PG8_SB(b, h) + boff + n * 2048 + k * 1024); } while (0)
; #define PG8_MMA(ai, bj, At, Bt) do { __builtin_amdgcn_s_setprio(1); _Pragma("unroll") for (int m = 0; m < 4; ++m) _Pragma("unroll") for (int n = 0; n < 2; ++n) _Pragma("unroll") for (int k = 0; k < 2; ++k) \
;         acc[ai][bj][m][n] = __builtin_amdgcn_mfma_f32_16x16x32_bf16(Bt[n][k], At[m][k], acc[ai][bj][m][n], 0, 0, 0); __builtin_amdgcn_s_setprio(0); } while (0)
; #define PG8_WAIT_V(n) asm volatile("s_waitcnt vmcnt(" #n ")" ::: "memory")
; #define PG8_WAIT_L(n) asm volatile("s_waitcnt lgkmcnt(" #n ")" ::: "memory")
; #define PG8_BAR __builtin_amdgcn_s_barrier()
; #define PG8_SCHED __builtin_amdgcn_sched_barrier(0)
; template <class Epi, class Sched>
; __device__ __forceinline__ void gemm_phase(LAS unsigned char* lds, const bf16_t* Abase, const int K, const Sched& S, const Epi& E, const int wvid) {
;     ...
;             const char* a2 = last ? Ab : Ab + (size_t)(t + 2) * kstep; const char* b2 = last ? nB : cB + (size_t)(t + 2) * kstep;
;             const char* a3 = a2 + kstep; const char* b3 = b2 + kstep;
;             PG8_LDB(B1, 0, 1); PG8_STAGE(PG8_SB(0, 0), b2, voffB);
;             PG8_BAR; PG8_WAIT_L(0); PG8_MMA(0, 1, At, B1); PG8_BAR;
;             PG8_LDA(At, 0, 1); PG8_STAGE(PG8_SA(0, 0), a2, voffA[0]);
;             PG8_BAR; PG8_WAIT_L(0); PG8_MMA(1, 0, At, B0); PG8_BAR; PG8_SCHED;
;             PG8_STAGE(PG8_SB(0, 1), b2 + hstep, voffB);
;             PG8_WAIT_V(6); PG8_BAR; PG8_MMA(1, 1, At, B1); PG8_BAR;
;             PG8_LDB(B0, 1, 0); PG8_SCHED; PG8_LDA(At, 1, 0); PG8_STAGE(PG8_SA(0, 1), a2, voffA[1]);
.LBB0_1479:
	s_add_u32 s28, s26, 0x100
	s_addc_u32 s29, s27, 0
	s_and_b64 s[30:31], s[4:5], exec
	s_cselect_b32 s30, 0, s28
	s_cselect_b32 s31, 0, s29
	s_add_u32 s30, s10, s30
	v_lshl_add_u64 v[236:237], v[196:197], 0, s[26:27]
	s_addc_u32 s31, s11, s31
	s_add_i32 s26, 0, 0x14000
	v_cndmask_b32_e64 v237, v237, v191, s[4:5]
	v_cndmask_b32_e64 v236, v236, v229, s[4:5]
	s_mov_b32 m0, s39
	v_add_u32_e32 v185, s26, v223
	v_lshl_add_u64 v[238:239], v[236:237], 0, v[180:181]
	ds_read_b128 v[200:203], v185
	ds_read_b128 v[206:209], v185 offset:1024
	ds_read_b128 v[210:213], v185 offset:2048
	ds_read_b128 v[232:235], v185 offset:3072
	global_load_lds_dwordx4 v[238:239], off
	v_lshl_add_u64 v[240:241], v[236:237], 0, v[182:183]
	s_mov_b32 m0, s42
	s_nop 0
	global_load_lds_dwordx4 v[240:241], off
	s_barrier
	s_waitcnt lgkmcnt(0)
	s_waitcnt lgkmcnt(0)
	v_mfma_f32_16x16x32_bf16 v[94:97], v[200:203], v[170:173], v[94:97]
	v_mfma_f32_16x16x32_bf16 v[90:93], v[210:213], v[170:173], v[90:93]
	v_mfma_f32_16x16x32_bf16 v[86:89], v[200:203], v[162:165], v[86:89]
	v_mfma_f32_16x16x32_bf16 v[82:85], v[210:213], v[162:165], v[82:85]
	v_mfma_f32_16x16x32_bf16 v[78:81], v[200:203], v[154:157], v[78:81]
	v_mfma_f32_16x16x32_bf16 v[74:77], v[210:213], v[154:157], v[74:77]
	v_mfma_f32_16x16x32_bf16 v[70:73], v[200:203], v[146:149], v[70:73]
	v_mfma_f32_16x16x32_bf16 v[66:69], v[210:213], v[146:149], v[66:69]
	v_mfma_f32_16x16x32_bf16 v[94:97], v[206:209], v[174:177], v[94:97]
	v_mfma_f32_16x16x32_bf16 v[90:93], v[232:235], v[174:177], v[90:93]
	v_mfma_f32_16x16x32_bf16 v[86:89], v[206:209], v[166:169], v[86:89]
	v_mfma_f32_16x16x32_bf16 v[82:85], v[232:235], v[166:169], v[82:85]
	v_mfma_f32_16x16x32_bf16 v[78:81], v[206:209], v[158:161], v[78:81]
	v_mfma_f32_16x16x32_bf16 v[74:77], v[232:235], v[158:161], v[74:77]
	v_mfma_f32_16x16x32_bf16 v[70:73], v[206:209], v[150:153], v[70:73]
	v_mfma_f32_16x16x32_bf16 v[66:69], v[232:235], v[150:153], v[66:69]
	s_mov_b32 m0, s17
	s_barrier
	ds_read_b128 v[146:149], v225 offset:16384
	ds_read_b128 v[150:153], v225 offset:17408
	ds_read_b128 v[154:157], v225 offset:18432
	ds_read_b128 v[158:161], v225 offset:19456
	ds_read_b128 v[162:165], v225 offset:20480
	ds_read_b128 v[166:169], v225 offset:21504
	ds_read_b128 v[170:173], v225 offset:22528
	ds_read_b128 v[174:177], v225 offset:23552
	global_load_lds_dwordx4 v0, s[30:31]
	s_mov_b32 m0, s43
	v_mov_b32_e32 v187, v1
	global_load_lds_dwordx4 v186, s[30:31]
	s_barrier
	s_waitcnt lgkmcnt(0)
	v_lshl_add_u64 v[242:243], s[30:31], 0, v[0:1]
	v_lshl_add_u64 v[244:245], s[30:31], 0, v[186:187]
	s_waitcnt lgkmcnt(0)
	v_mfma_f32_16x16x32_bf16 v[62:65], v[130:133], v[146:149], v[62:65]
	v_mfma_f32_16x16x32_bf16 v[58:61], v[138:141], v[146:149], v[58:61]
	v_mfma_f32_16x16x32_bf16 v[46:49], v[130:133], v[154:157], v[46:49]
	v_mfma_f32_16x16x32_bf16 v[42:45], v[138:141], v[154:157], v[42:45]
	v_mfma_f32_16x16x32_bf16 v[30:33], v[130:133], v[162:165], v[30:33]
	v_mfma_f32_16x16x32_bf16 v[26:29], v[138:141], v[162:165], v[26:29]
	v_mfma_f32_16x16x32_bf16 v[14:17], v[130:133], v[170:173], v[14:17]
	v_mfma_f32_16x16x32_bf16 v[10:13], v[138:141], v[170:173], v[10:13]
	v_mfma_f32_16x16x32_bf16 v[62:65], v[134:137], v[150:153], v[62:65]
	v_mfma_f32_16x16x32_bf16 v[58:61], v[142:145], v[150:153], v[58:61]
	v_mfma_f32_16x16x32_bf16 v[46:49], v[134:137], v[158:161], v[46:49]
	v_mfma_f32_16x16x32_bf16 v[42:45], v[142:145], v[158:161], v[42:45]
	v_mfma_f32_16x16x32_bf16 v[30:33], v[134:137], v[166:169], v[30:33]
	v_mfma_f32_16x16x32_bf16 v[26:29], v[142:145], v[166:169], v[26:29]
	v_mfma_f32_16x16x32_bf16 v[14:17], v[134:137], v[174:177], v[14:17]
	v_mfma_f32_16x16x32_bf16 v[10:13], v[142:145], v[174:177], v[10:13]
	s_barrier
	v_lshl_add_u64 v[130:131], v[236:237], 0, s[68:69]
	s_add_i32 s4, s26, s38
	v_lshl_add_u64 v[132:133], v[130:131], 0, v[180:181]
	s_mov_b32 m0, s4
	v_lshl_add_u64 v[130:131], v[130:131], 0, v[182:183]
	global_load_lds_dwordx4 v[132:133], off
	s_add_i32 m0, s4, 0x2000
	s_nop 0
	global_load_lds_dwordx4 v[130:131], off
	s_waitcnt vmcnt(6)
	s_barrier
	v_mfma_f32_16x16x32_bf16 v[54:57], v[200:203], v[146:149], v[54:57]
	v_mfma_f32_16x16x32_bf16 v[50:53], v[210:213], v[146:149], v[50:53]
	v_mfma_f32_16x16x32_bf16 v[38:41], v[200:203], v[154:157], v[38:41]
	v_mfma_f32_16x16x32_bf16 v[34:37], v[210:213], v[154:157], v[34:37]
	v_mfma_f32_16x16x32_bf16 v[22:25], v[200:203], v[162:165], v[22:25]
	v_mfma_f32_16x16x32_bf16 v[18:21], v[210:213], v[162:165], v[18:21]
	v_mfma_f32_16x16x32_bf16 v[6:9], v[200:203], v[170:173], v[6:9]
	v_mfma_f32_16x16x32_bf16 v[2:5], v[210:213], v[170:173], v[2:5]
	v_mfma_f32_16x16x32_bf16 v[54:57], v[206:209], v[150:153], v[54:57]
	v_mfma_f32_16x16x32_bf16 v[50:53], v[232:235], v[150:153], v[50:53]
	v_mfma_f32_16x16x32_bf16 v[38:41], v[206:209], v[158:161], v[38:41]
	v_mfma_f32_16x16x32_bf16 v[34:37], v[232:235], v[158:161], v[34:37]
	v_mfma_f32_16x16x32_bf16 v[22:25], v[206:209], v[166:169], v[22:25]
	v_mfma_f32_16x16x32_bf16 v[18:21], v[232:235], v[166:169], v[18:21]
	v_mfma_f32_16x16x32_bf16 v[6:9], v[206:209], v[174:177], v[6:9]
	v_mfma_f32_16x16x32_bf16 v[2:5], v[232:235], v[174:177], v[2:5]
	s_add_i32 s4, 0, 0x18000
	v_add_u32_e32 v142, s4, v223
	s_barrier
	ds_read_b128 v[130:133], v142
	ds_read_b128 v[134:137], v142 offset:1024
	ds_read_b128 v[138:141], v142 offset:2048
	ds_read_b128 v[142:145], v142 offset:3072
	s_mov_b32 m0, s46
	v_lshl_add_u64 v[198:199], s[30:31], 0, v[198:199]
	ds_read_b128 v[146:149], v225 offset:32768
	ds_read_b128 v[150:153], v225 offset:33792
	ds_read_b128 v[154:157], v225 offset:34816
	ds_read_b128 v[158:161], v225 offset:35840
	ds_read_b128 v[162:165], v225 offset:36864
	ds_read_b128 v[166:169], v225 offset:37888
	ds_read_b128 v[170:173], v225 offset:38912
	ds_read_b128 v[174:177], v225 offset:39936
	global_load_lds_dwordx4 v[198:199], off
	v_lshl_add_u64 v[198:199], s[30:31], 0, v[188:189]
	s_mov_b32 m0, s47
	s_nop 0
	global_load_lds_dwordx4 v[198:199], off
	s_waitcnt lgkmcnt(8)
	s_barrier
; #define PG8_STAGE(bufoff, gbase, voff) do { _Pragma("unroll") for (int _i = 0; _i < 2; ++_i) \
;         __builtin_amdgcn_global_load_lds((const unsigned*)((const char*)(gbase) + (voff)[_i]), (LAS unsigned*)(lds + (bufoff) + ldsw + _i * 8192), 16, 0, 0); } while (0)
; #define PG8_LDA(dst, b, h) do { _Pragma("unroll") for (int m = 0; m < 4; ++m) _Pragma("unroll") for (int k = 0; k < 2; ++k) dst[m][k] = *(const LAS bf16x8*)(lds + PG8_SA(b, h) + aoff + m * 2048 + k * 1024); } while (0)
; #define PG8_LDB(dst, b, h) do { _Pragma("unroll") for (int n = 0; n < 2; ++n) _Pragma("unroll") for (int k = 0; k < 2; ++k) dst[n][k] = *(const LAS bf16x8*)(lds + PG8_SB(b, h) + boff + n * 2048 + k * 1024); } while (0)
; #define PG8_MMA(ai, bj, At, Bt) do { __builtin_amdgcn_s_setprio(1); _Pragma("unroll") for (int m = 0; m < 4; ++m) _Pragma("unroll") for (int n = 0; n < 2; ++n) _Pragma("unroll") for (int k = 0; k < 2; ++k) \
;         acc[ai][bj][m][n] = __builtin_amdgcn_mfma_f32_16x16x32_bf16(Bt[n][k], At[m][k], acc[ai][bj][m][n], 0, 0, 0); __builtin_amdgcn_s_setprio(0); } while (0)
; #define PG8_WAIT_V(n) asm volatile("s_waitcnt vmcnt(" #n ")" ::: "memory")
; #define PG8_WAIT_L(n) asm volatile("s_waitcnt lgkmcnt(" #n ")" ::: "memory")
; #define PG8_BAR __builtin_amdgcn_s_barrier()
; #define PG8_SCHED __builtin_amdgcn_sched_barrier(0)
; template <class Epi, class Sched>
; __device__ __forceinline__ void gemm_phase(LAS unsigned char* lds, const bf16_t* Abase, const int K, const Sched& S, const Epi& E, const int wvid) {
;     ...
;             PG8_WAIT_L(8); PG8_BAR; PG8_WAIT_L(0); PG8_MMA(0, 0, At, B0); PG8_BAR; PG8_SCHED;
;             PG8_LDB(B1, 1, 1); PG8_STAGE(PG8_SB(1, 0), b3, voffB);
;             PG8_BAR; PG8_WAIT_L(0); PG8_MMA(0, 1, At, B1); PG8_BAR;
;             PG8_LDA(At, 1, 1); PG8_STAGE(PG8_SA(1, 0), a3, voffA[0]);
;             PG8_BAR; PG8_WAIT_L(0); PG8_MMA(1, 0, At, B0); PG8_BAR; PG8_SCHED;
;             PG8_STAGE(PG8_SB(1, 1), b3 + hstep, voffB);
;             PG8_WAIT_V(6); PG8_BAR; PG8_MMA(1, 1, At, B1); PG8_BAR;
;         }
	s_waitcnt lgkmcnt(0)
	s_waitcnt lgkmcnt(0)
	v_mfma_f32_16x16x32_bf16 v[126:129], v[130:133], v[146:149], v[126:129]
	v_mfma_f32_16x16x32_bf16 v[122:125], v[138:141], v[146:149], v[122:125]
	v_mfma_f32_16x16x32_bf16 v[118:121], v[130:133], v[154:157], v[118:121]
	v_mfma_f32_16x16x32_bf16 v[114:117], v[138:141], v[154:157], v[114:117]
	v_mfma_f32_16x16x32_bf16 v[110:113], v[130:133], v[162:165], v[110:113]
	v_mfma_f32_16x16x32_bf16 v[106:109], v[138:141], v[162:165], v[106:109]
	v_mfma_f32_16x16x32_bf16 v[102:105], v[130:133], v[170:173], v[102:105]
	v_mfma_f32_16x16x32_bf16 v[98:101], v[138:141], v[170:173], v[98:101]
	v_mfma_f32_16x16x32_bf16 v[126:129], v[134:137], v[150:153], v[126:129]
	v_mfma_f32_16x16x32_bf16 v[122:125], v[142:145], v[150:153], v[122:125]
	v_mfma_f32_16x16x32_bf16 v[118:121], v[134:137], v[158:161], v[118:121]
	v_mfma_f32_16x16x32_bf16 v[114:117], v[142:145], v[158:161], v[114:117]
	v_mfma_f32_16x16x32_bf16 v[110:113], v[134:137], v[166:169], v[110:113]
	v_mfma_f32_16x16x32_bf16 v[106:109], v[142:145], v[166:169], v[106:109]
	v_mfma_f32_16x16x32_bf16 v[102:105], v[134:137], v[174:177], v[102:105]
	v_mfma_f32_16x16x32_bf16 v[98:101], v[142:145], v[174:177], v[98:101]
	s_barrier
	s_add_i32 s5, 0, 0x1c000
	s_add_i32 s4, s4, s38
	v_add_u32_e32 v185, s5, v223
	v_lshl_add_u64 v[202:203], v[238:239], 0, s[12:13]
	s_mov_b32 m0, s4
	ds_read_b128 v[198:201], v185
	ds_read_b128 v[206:209], v185 offset:1024
	ds_read_b128 v[210:213], v185 offset:2048
	ds_read_b128 v[232:235], v185 offset:3072
	global_load_lds_dwordx4 v[202:203], off
	v_lshl_add_u64 v[202:203], v[240:241], 0, s[12:13]
	s_add_i32 m0, s4, 0x2000
	s_nop 0
	global_load_lds_dwordx4 v[202:203], off
	s_barrier
	s_waitcnt lgkmcnt(0)
	s_waitcnt lgkmcnt(0)
	v_mfma_f32_16x16x32_bf16 v[94:97], v[198:201], v[146:149], v[94:97]
	v_mfma_f32_16x16x32_bf16 v[90:93], v[210:213], v[146:149], v[90:93]
	v_mfma_f32_16x16x32_bf16 v[86:89], v[198:201], v[154:157], v[86:89]
	v_mfma_f32_16x16x32_bf16 v[82:85], v[210:213], v[154:157], v[82:85]
	v_mfma_f32_16x16x32_bf16 v[78:81], v[198:201], v[162:165], v[78:81]
	v_mfma_f32_16x16x32_bf16 v[74:77], v[210:213], v[162:165], v[74:77]
	v_mfma_f32_16x16x32_bf16 v[70:73], v[198:201], v[170:173], v[70:73]
	v_mfma_f32_16x16x32_bf16 v[66:69], v[210:213], v[170:173], v[66:69]
	v_mfma_f32_16x16x32_bf16 v[94:97], v[206:209], v[150:153], v[94:97]
	v_mfma_f32_16x16x32_bf16 v[90:93], v[232:235], v[150:153], v[90:93]
	v_mfma_f32_16x16x32_bf16 v[86:89], v[206:209], v[158:161], v[86:89]
	v_mfma_f32_16x16x32_bf16 v[82:85], v[232:235], v[158:161], v[82:85]
	v_mfma_f32_16x16x32_bf16 v[78:81], v[206:209], v[166:169], v[78:81]
	v_mfma_f32_16x16x32_bf16 v[74:77], v[232:235], v[166:169], v[74:77]
	v_mfma_f32_16x16x32_bf16 v[70:73], v[206:209], v[174:177], v[70:73]
	v_mfma_f32_16x16x32_bf16 v[66:69], v[232:235], v[174:177], v[66:69]
	s_mov_b32 m0, s48
	v_lshl_add_u64 v[202:203], v[242:243], 0, s[12:13]
	s_barrier
	ds_read_b128 v[146:149], v225 offset:49152
	ds_read_b128 v[150:153], v225 offset:50176
	ds_read_b128 v[154:157], v225 offset:51200
	ds_read_b128 v[158:161], v225 offset:52224
	ds_read_b128 v[162:165], v225 offset:53248
	ds_read_b128 v[166:169], v225 offset:54272
	ds_read_b128 v[170:173], v225 offset:55296
	ds_read_b128 v[174:177], v225 offset:56320
	global_load_lds_dwordx4 v[202:203], off
	v_lshl_add_u64 v[202:203], v[244:245], 0, s[12:13]
	s_mov_b32 m0, s49
	s_nop 0
	global_load_lds_dwordx4 v[202:203], off
	s_barrier
	s_waitcnt lgkmcnt(0)
	s_waitcnt lgkmcnt(0)
	v_mfma_f32_16x16x32_bf16 v[62:65], v[130:133], v[146:149], v[62:65]
	v_mfma_f32_16x16x32_bf16 v[58:61], v[138:141], v[146:149], v[58:61]
	v_mfma_f32_16x16x32_bf16 v[46:49], v[130:133], v[154:157], v[46:49]
	v_mfma_f32_16x16x32_bf16 v[42:45], v[138:141], v[154:157], v[42:45]
	v_mfma_f32_16x16x32_bf16 v[30:33], v[130:133], v[162:165], v[30:33]
	v_mfma_f32_16x16x32_bf16 v[26:29], v[138:141], v[162:165], v[26:29]
	v_mfma_f32_16x16x32_bf16 v[14:17], v[130:133], v[170:173], v[14:17]
	v_mfma_f32_16x16x32_bf16 v[10:13], v[138:141], v[170:173], v[10:13]
	v_mfma_f32_16x16x32_bf16 v[62:65], v[134:137], v[150:153], v[62:65]
	v_mfma_f32_16x16x32_bf16 v[58:61], v[142:145], v[150:153], v[58:61]
	v_mfma_f32_16x16x32_bf16 v[46:49], v[134:137], v[158:161], v[46:49]
	v_mfma_f32_16x16x32_bf16 v[42:45], v[142:145], v[158:161], v[42:45]
	v_mfma_f32_16x16x32_bf16 v[30:33], v[134:137], v[166:169], v[30:33]
	v_mfma_f32_16x16x32_bf16 v[26:29], v[142:145], v[166:169], v[26:29]
	v_mfma_f32_16x16x32_bf16 v[14:17], v[134:137], v[174:177], v[14:17]
	v_mfma_f32_16x16x32_bf16 v[10:13], v[142:145], v[174:177], v[10:13]
	s_barrier
	v_lshl_add_u64 v[130:131], v[236:237], 0, s[84:85]
	s_add_i32 s4, s5, s38
	v_lshl_add_u64 v[132:133], v[130:131], 0, v[180:181]
	s_mov_b32 m0, s4
	v_lshl_add_u64 v[130:131], v[130:131], 0, v[182:183]
	global_load_lds_dwordx4 v[132:133], off
	s_add_i32 m0, s4, 0x2000
	s_nop 0
	global_load_lds_dwordx4 v[130:131], off
	s_waitcnt vmcnt(6)
	s_barrier
	v_mfma_f32_16x16x32_bf16 v[54:57], v[198:201], v[146:149], v[54:57]
	v_mfma_f32_16x16x32_bf16 v[50:53], v[210:213], v[146:149], v[50:53]
	v_mfma_f32_16x16x32_bf16 v[38:41], v[198:201], v[154:157], v[38:41]
	v_mfma_f32_16x16x32_bf16 v[34:37], v[210:213], v[154:157], v[34:37]
	v_mfma_f32_16x16x32_bf16 v[22:25], v[198:201], v[162:165], v[22:25]
	v_mfma_f32_16x16x32_bf16 v[18:21], v[210:213], v[162:165], v[18:21]
	v_mfma_f32_16x16x32_bf16 v[6:9], v[198:201], v[170:173], v[6:9]
	v_mfma_f32_16x16x32_bf16 v[2:5], v[210:213], v[170:173], v[2:5]
	v_mfma_f32_16x16x32_bf16 v[54:57], v[206:209], v[150:153], v[54:57]
	v_mfma_f32_16x16x32_bf16 v[50:53], v[232:235], v[150:153], v[50:53]
	v_mfma_f32_16x16x32_bf16 v[38:41], v[206:209], v[158:161], v[38:41]
	v_mfma_f32_16x16x32_bf16 v[34:37], v[232:235], v[158:161], v[34:37]
	v_mfma_f32_16x16x32_bf16 v[22:25], v[206:209], v[166:169], v[22:25]
	v_mfma_f32_16x16x32_bf16 v[18:21], v[232:235], v[166:169], v[18:21]
	v_mfma_f32_16x16x32_bf16 v[6:9], v[206:209], v[174:177], v[6:9]
	v_mfma_f32_16x16x32_bf16 v[2:5], v[232:235], v[174:177], v[2:5]
	s_add_i32 s25, s25, 2
	s_cmp_gt_u32 s25, 5
	s_barrier
	s_cbranch_scc1 .LBB0_1481
	s_mov_b64 s[26:27], s[28:29]
	s_branch .LBB0_1476
